# fp8 expert weights in [k-block][row-group] 4KB-block layout (WG writes 32KB contiguous; GEMM B tile = one 32KB chunk per K-step) + write-through stores as in v15
# baseline (speedup 1.0000x reference)
; __device__ __forceinline__ MoeItem moe_item(const float* wg, const float* wu, const float* wd, const float* win, const float* wout, const float* wpn, const float* wpd, unsigned char* ws, int r, int lane) {
;     if (r >= NMOE_X + NGATE_IT + NWO_IT) { const int q = r - NMOE_X - NGATE_IT - NWO_IT, which = q >> 9, kb = (q >> 6) & 7, nb = q & 63; MoeItem it; it.stride = DM; it.dpitch = 1024;
;         it.src = (which ? wpd : wpn) + (size_t)(kb * 128 + (lane >> 5)) * DM + nb * 32 + (lane & 31);
;         it.dst = ws + (which ? WS_WPDFT : WS_WPNAT) + (size_t)(nb * 32) * 1024 + kb * 128 + (size_t)(lane >> 3) * 1024 + 16 * (lane & 7); return it; }
;     if (r >= NMOE_X + NGATE_IT) { const int q = r - NMOE_X - NGATE_IT, kb = q >> 6, nb = q & 63; MoeItem it; it.stride = DM; it.dpitch = DM;
;         it.src = wout + (size_t)(kb * 128 + (lane >> 5)) * DM + nb * 32 + (lane & 31);
;         it.dst = ws + WS_WO8 + (size_t)(nb * 32) * DM + kb * 128 + (size_t)(lane >> 3) * DM + 16 * (lane & 7); return it; }
;     if (r >= NMOE_X) { const int q = r - NMOE_X, kb = q / 192, nb = q % 192; MoeItem it; it.stride = INC; it.dpitch = DM;
;         const int scol = nb < 128 ? 6144 + nb * 32 : (nb < 160 ? 1024 + (nb - 128) * 32 : 3072 + (nb - 160) * 32);
;         it.src = win + (size_t)(kb * 128 + (lane >> 5)) * INC + scol + (lane & 31);
;         it.dst = ws + WS_WG8 + (size_t)(nb * 32) * DM + kb * 128 + (size_t)(lane >> 3) * DM + 16 * (lane & 7); return it; }
;     const int mat = r / MOE_IE, q = r % MOE_IE, e = mat / 3, which = mat % 3, kb = q / 64, nb = q % 64, n0 = nb * 32;
;     const float* src = (which == 0 ? wg : (which == 1 ? wu : wd)) + (size_t)e * DM * DFF + (size_t)(kb * 128 + (lane >> 5)) * DFF + n0 + (lane & 31);
;     unsigned char* dst;
;     if (which < 2) dst = ws + WS_WGUT + ((size_t)(e * 16 + (n0 >> 7)) * 256 + which * 128 + (n0 & 127)) * DM;
;     else dst = ws + WS_WDT + ((size_t)e * DM + n0) * DFF;
;     MoeItem it; it.stride = DFF; it.dpitch = DM; it.src = src; it.dst = dst + kb * 128 + (size_t)(lane >> 3) * DM + 16 * (lane & 7); return it;
;     ...
;         const int nmine = (NMOE - gw + NGW - 1) / NGW;
;         const int last = gw + (nmine - 1) * NGW;
;         MoeItem ia = moe_item(wg, wu, wd, win, wout, wpn, wpd, F.ws, gw, F.lane), ib = ia;
.LBB0_49:
	s_mov_b32 s32, 0
	s_abs_i32 s6, s72
	v_cvt_f32_u32_e32 v1, s6
	s_sub_i32 s4, s72, s3
	s_add_i32 s68, s4, 0x193ff
	s_sub_i32 s4, 0xfffe6c01, s4
	v_rcp_iflag_f32_e32 v1, v1
	s_max_i32 s7, s68, s4
	s_sub_i32 s4, 0, s6
	v_mul_f32_e32 v1, 0x4f7ffffe, v1
	v_cvt_u32_f32_e32 v1, v1
	s_nop 0
	v_readfirstlane_b32 s5, v1
	s_mul_i32 s4, s4, s5
	s_mul_hi_u32 s4, s5, s4
	s_add_i32 s5, s5, s4
	s_cmp_lt_i32 s3, 0x19000
	s_mul_hi_u32 s47, s7, s5
	s_cbranch_scc0 .LBB0_54
	s_cmp_lt_i32 s3, 0x18c00
	s_cbranch_scc0 .LBB0_56
	s_cmp_lt_i32 s3, 0x18000
	s_cbranch_scc0 .LBB0_57
	s_mov_b32 s32, 1
	s_ashr_i32 s4, s3, 31
	s_lshr_b32 s4, s4, 22
	s_add_i32 s4, s3, s4
	s_ashr_i32 s5, s4, 10
	s_and_b32 s4, s4, 0xfc00
	s_sub_i32 s38, s3, s4
	s_mul_hi_i32 s4, s3, 0x2aaaaaab
	s_lshr_b32 s39, s4, 31
	s_ashr_i32 s4, s4, 9
	s_add_i32 s4, s4, s39
	s_mul_hi_i32 s39, s5, 0x55555556
	s_lshr_b32 s42, s39, 31
	s_add_i32 s39, s39, s42
	s_mul_i32 s39, s39, 3
	s_sub_i32 s69, s5, s39
	s_sext_i32_i16 s5, s38
	s_bfe_u32 s5, s5, 0x60019
	s_add_i32 s42, s38, s5
	s_and_b32 s5, s42, 0xffc0
	s_sub_i32 s5, s38, s5
	s_sext_i32_i16 s70, s5
	s_lshl_b32 s38, s70, 5
	s_ashr_i32 s5, s4, 31
	s_ashr_i32 s39, s38, 31
	s_cmp_gt_i32 s69, 1
	s_sext_i32_i16 s71, s42
	s_cbranch_scc0 .LBB0_58
	s_mov_b32 s99, 16
	s_lshl_b64 s[42:43], s[4:5], 18
	s_lshl_b64 s[44:45], s[38:39], 7
	s_add_u32 s42, s82, s42
	s_addc_u32 s43, s83, s43
	s_add_u32 s42, s42, s44
	s_addc_u32 s43, s43, s45
	s_add_u32 s42, s42, 0x24000000
	s_addc_u32 s43, s43, 0
	s_mov_b64 s[44:45], 0
	s_branch .LBB0_59

; __device__ __forceinline__ MoeItem moe_item(const float* wg, const float* wu, const float* wd, const float* win, const float* wout, const float* wpn, const float* wpd, unsigned char* ws, int r, int lane) {
;     ...
;     const int mat = r / MOE_IE, q = r % MOE_IE, e = mat / 3, which = mat % 3, kb = q / 64, nb = q % 64, n0 = nb * 32;
;     const float* src = (which == 0 ? wg : (which == 1 ? wu : wd)) + (size_t)e * DM * DFF + (size_t)(kb * 128 + (lane >> 5)) * DFF + n0 + (lane & 31);
;     unsigned char* dst;
;     if (which < 2) dst = ws + WS_WGUT + ((size_t)(e * 16 + (n0 >> 7)) * 256 + which * 128 + (n0 & 127)) * DM;
;     else dst = ws + WS_WDT + ((size_t)e * DM + n0) * DFF;
;     MoeItem it; it.stride = DFF; it.dpitch = DM; it.src = src; it.dst = dst + kb * 128 + (size_t)(lane >> 3) * DM + 16 * (lane & 7); return it;
.LBB0_59:
	s_andn2_b64 vcc, exec, s[44:45]
	s_lshr_b32 s44, s71, 6
	s_cbranch_vccnz .LBB0_61
	s_lshl_b32 s42, s4, 4
	s_ashr_i32 s43, s70, 2
	s_add_i32 s42, s43, s42
	s_ashr_i32 s43, s42, 31
	s_lshl_b32 s45, s69, 7
	s_lshl_b64 s[42:43], s[42:43], 8
	s_ashr_i32 s70, s45, 31
	s_add_u32 s42, s42, s45
	s_addc_u32 s43, s43, s70
	s_and_b32 s45, s38, 0x60
	s_or_b32 s42, s42, s45
	s_mov_b32 s99, 17
	s_lshl_b64 s[42:43], s[42:43], 7
	s_add_u32 s42, s82, s42
	s_addc_u32 s43, s83, s43
	s_add_u32 s42, s42, 0x4000000
	s_addc_u32 s43, s43, 0
.LBB0_61:
	s_cmp_eq_u32 s69, 1
	s_cselect_b32 s45, s20, s24
	s_cselect_b32 s70, s21, s25
	s_cmp_eq_u32 s69, 0
	s_cselect_b32 s69, s17, s70
	s_cselect_b32 s45, s16, s45
	s_lshl_b64 s[4:5], s[4:5], 24
	s_sext_i32_i16 s44, s44
	s_add_u32 s4, s45, s4
	s_addc_u32 s5, s69, s5
	s_lshl_b32 s44, s44, 7
	v_lshrrev_b32_e32 v1, 5, v170
	v_or_b32_e32 v4, s44, v1
	v_ashrrev_i32_e32 v5, 31, v4
	v_lshlrev_b64 v[4:5], 13, v[4:5]
	v_lshl_add_u64 v[4:5], s[4:5], 0, v[4:5]
	s_ashr_i32 s4, s44, 31
	v_lshl_add_u64 v[4:5], s[38:39], 2, v[4:5]
	v_and_b32_e32 v1, 31, v0
	s_lshl_b32 s98, s44, s99
	s_add_u32 s38, s42, s98
	v_lshlrev_b32_e32 v6, 2, v1
	v_mov_b32_e32 v7, 0
	s_addc_u32 s39, s43, s4
	v_lshl_add_u64 v[4:5], v[4:5], 0, v[6:7]
	v_mov_b64_e32 v[6:7], s[38:39]
	s_mov_b64 s[44:45], 0x800
	s_branch .LBB0_73

; __device__ __forceinline__ MoeItem moe_item(const float* wg, const float* wu, const float* wd, const float* win, const float* wout, const float* wpn, const float* wpd, unsigned char* ws, int r, int lane) {
;     if (r >= NMOE_X + NGATE_IT + NWO_IT) { const int q = r - NMOE_X - NGATE_IT - NWO_IT, which = q >> 9, kb = (q >> 6) & 7, nb = q & 63; MoeItem it; it.stride = DM; it.dpitch = 1024;
;         it.src = (which ? wpd : wpn) + (size_t)(kb * 128 + (lane >> 5)) * DM + nb * 32 + (lane & 31);
;         it.dst = ws + (which ? WS_WPDFT : WS_WPNAT) + (size_t)(nb * 32) * 1024 + kb * 128 + (size_t)(lane >> 3) * 1024 + 16 * (lane & 7); return it; }
;     if (r >= NMOE_X + NGATE_IT) { const int q = r - NMOE_X - NGATE_IT, kb = q >> 6, nb = q & 63; MoeItem it; it.stride = DM; it.dpitch = DM;
;         it.src = wout + (size_t)(kb * 128 + (lane >> 5)) * DM + nb * 32 + (lane & 31);
;         it.dst = ws + WS_WO8 + (size_t)(nb * 32) * DM + kb * 128 + (size_t)(lane >> 3) * DM + 16 * (lane & 7); return it; }
;     if (r >= NMOE_X) { const int q = r - NMOE_X, kb = q / 192, nb = q % 192; MoeItem it; it.stride = INC; it.dpitch = DM;
;         const int scol = nb < 128 ? 6144 + nb * 32 : (nb < 160 ? 1024 + (nb - 128) * 32 : 3072 + (nb - 160) * 32);
;         it.src = win + (size_t)(kb * 128 + (lane >> 5)) * INC + scol + (lane & 31);
;         it.dst = ws + WS_WG8 + (size_t)(nb * 32) * DM + kb * 128 + (size_t)(lane >> 3) * DM + 16 * (lane & 7); return it; }
;     const int mat = r / MOE_IE, q = r % MOE_IE, e = mat / 3, which = mat % 3, kb = q / 64, nb = q % 64, n0 = nb * 32;
;     const float* src = (which == 0 ? wg : (which == 1 ? wu : wd)) + (size_t)e * DM * DFF + (size_t)(kb * 128 + (lane >> 5)) * DFF + n0 + (lane & 31);
;     unsigned char* dst;
;     if (which < 2) dst = ws + WS_WGUT + ((size_t)(e * 16 + (n0 >> 7)) * 256 + which * 128 + (n0 & 127)) * DM;
;     else dst = ws + WS_WDT + ((size_t)e * DM + n0) * DFF;
;     MoeItem it; it.stride = DFF; it.dpitch = DM; it.src = src; it.dst = dst + kb * 128 + (size_t)(lane >> 3) * DM + 16 * (lane & 7); return it;
;     ...
;             const int it1 = gw + (j + 1) * NGW, it2 = gw + (j + 2) * NGW;
;             ib = moe_item(wg, wu, wd, win, wout, wpn, wpd, F.ws, it1 <= last ? it1 : last, F.lane); MOE_LOAD(vb, ib);
.LBB0_81:
	s_mov_b32 s92, 0
	s_add_i32 s4, s72, s3
	s_min_i32 s70, s4, s7
	s_cmp_lt_i32 s70, 0x19000
	s_mov_b64 s[42:43], -1
	s_cbranch_scc0 .LBB0_102
	s_cmp_lt_i32 s70, 0x18c00
	s_cbranch_scc0 .LBB0_99
	s_cmp_lt_i32 s70, 0x18000
	s_cbranch_scc0 .LBB0_89
	s_mov_b32 s92, 1
	s_ashr_i32 s4, s70, 31
	s_lshr_b32 s4, s4, 22
	s_add_i32 s4, s70, s4
	s_ashr_i32 s43, s4, 10
	s_and_b32 s4, s4, 0xfc00
	s_sub_i32 s44, s70, s4
	s_mul_hi_i32 s4, s70, 0x2aaaaaab
	s_lshr_b32 s42, s4, 31
	s_ashr_i32 s4, s4, 9
	s_add_i32 s42, s4, s42
	s_mul_hi_i32 s4, s43, 0x55555556
	s_lshr_b32 s45, s4, 31
	s_add_i32 s4, s4, s45
	s_mul_i32 s4, s4, 3
	s_sub_i32 s4, s43, s4
	s_sext_i32_i16 s43, s44
	s_bfe_u32 s43, s43, 0x60019
	s_add_i32 s71, s44, s43
	s_and_b32 s43, s71, 0xffc0
	s_sub_i32 s43, s44, s43
	s_sext_i32_i16 s84, s43
	s_lshl_b32 s44, s84, 5
	s_ashr_i32 s43, s42, 31
	s_ashr_i32 s45, s44, 31
	s_cmp_gt_i32 s4, 1
	s_mov_b64 s[68:69], -1
	s_cbranch_scc0 .LBB0_86
	s_mov_b32 s99, 16
	s_lshl_b64 s[46:47], s[42:43], 18
	s_lshl_b64 s[68:69], s[44:45], 7
	s_add_u32 s46, s73, s46
	s_addc_u32 s47, s74, s47
	s_add_u32 s46, s46, s68
	s_addc_u32 s47, s47, s69
	s_mov_b64 s[68:69], 0
.LBB0_86:
	s_andn2_b64 vcc, exec, s[68:69]
	s_cbranch_vccnz .LBB0_88
	s_lshl_b32 s46, s42, 4
	s_ashr_i32 s47, s84, 2
	s_add_i32 s46, s47, s46
	s_ashr_i32 s47, s46, 31
	s_lshl_b32 s68, s4, 7
	s_lshl_b64 s[46:47], s[46:47], 8
	s_ashr_i32 s69, s68, 31
	s_add_u32 s46, s46, s68
	s_addc_u32 s47, s47, s69
	s_and_b32 s68, s44, 0x60
	s_or_b32 s46, s46, s68
	s_mov_b32 s99, 17
	s_lshl_b64 s[46:47], s[46:47], 7
	s_add_u32 s46, s75, s46
	s_addc_u32 s47, s76, s47
.LBB0_88:
	s_sext_i32_i16 s68, s71
	s_lshr_b32 s68, s68, 6
	s_cmp_eq_u32 s4, 1
	s_cselect_b32 s69, s20, s24
	s_cselect_b32 s71, s21, s25
	s_cmp_eq_u32 s4, 0
	s_cselect_b32 s4, s17, s71
	s_cselect_b32 s69, s16, s69
	s_lshl_b64 s[42:43], s[42:43], 24
	s_sext_i32_i16 s68, s68
	s_add_u32 s42, s69, s42
	s_addc_u32 s43, s4, s43
	s_lshl_b32 s4, s68, 7
	v_or_b32_e32 v12, s4, v20
	v_ashrrev_i32_e32 v13, 31, v12
	v_lshlrev_b64 v[12:13], 13, v[12:13]
	v_lshl_add_u64 v[12:13], s[42:43], 0, v[12:13]
	s_ashr_i32 s42, s4, 31
	v_lshl_add_u64 v[12:13], s[44:45], 2, v[12:13]
	s_lshl_b32 s98, s4, s99
	s_add_u32 s44, s46, s98
	v_lshlrev_b32_e32 v4, 2, v8
	s_addc_u32 s45, s47, s42
	v_lshl_add_u64 v[16:17], v[12:13], 0, v[4:5]
	s_mov_b64 s[42:43], 0
	v_mov_b64_e32 v[12:13], s[44:45]

; #define MOE_LOAD(v, it) do { _Pragma("unroll") for (int i_ = 0; i_ < 64; ++i_) v[i_] = __builtin_nontemporal_load((it).src + (size_t)(2 * i_) * (it).stride); } while (0)
;     ...
;             ia = moe_item(wg, wu, wd, win, wout, wpn, wpd, F.ws, it2 <= last ? it2 : last, F.lane); MOE_LOAD(va, ia);
;             MOE_PROC(vb, ib);
.LBB0_105:
	s_lshl_b64 s[46:47], s[46:47], 3
	global_load_dword v93, v[16:17], off nt
	v_lshl_add_u64 v[16:17], v[16:17], 0, s[46:47]
	v_lshl_add_u64 v[94:95], v[16:17], 0, s[46:47]
	v_lshl_add_u64 v[96:97], v[94:95], 0, s[46:47]
	v_lshl_add_u64 v[102:103], v[96:97], 0, s[46:47]
	v_lshl_add_u64 v[104:105], v[102:103], 0, s[46:47]
	v_lshl_add_u64 v[106:107], v[104:105], 0, s[46:47]
	v_lshl_add_u64 v[108:109], v[106:107], 0, s[46:47]
	v_lshl_add_u64 v[110:111], v[108:109], 0, s[46:47]
	global_load_dword v101, v[16:17], off nt
	global_load_dword v99, v[94:95], off nt
	global_load_dword v100, v[96:97], off nt
	s_nop 0
	global_load_dword v97, v[102:103], off nt
	global_load_dword v98, v[104:105], off nt
	global_load_dword v95, v[106:107], off nt
	global_load_dword v96, v[108:109], off nt
	global_load_dword v94, v[110:111], off nt
	v_lshl_add_u64 v[16:17], v[110:111], 0, s[46:47]
	s_waitcnt vmcnt(9)
	ds_write2st64_b32 v28, v87, v92 offset1:1
	v_lshl_add_u64 v[102:103], v[16:17], 0, s[46:47]
	global_load_dword v124, v[16:17], off nt
	global_load_dword v104, v[102:103], off nt
	v_lshl_add_u64 v[16:17], v[102:103], 0, s[46:47]
	global_load_dword v114, v[16:17], off nt
	v_lshl_add_u64 v[16:17], v[16:17], 0, s[46:47]
	global_load_dword v105, v[16:17], off nt
	v_lshl_add_u64 v[16:17], v[16:17], 0, s[46:47]
	global_load_dword v115, v[16:17], off nt
	v_lshl_add_u64 v[16:17], v[16:17], 0, s[46:47]
	global_load_dword v106, v[16:17], off nt
	v_lshl_add_u64 v[16:17], v[16:17], 0, s[46:47]
	global_load_dword v116, v[16:17], off nt
	v_lshl_add_u64 v[16:17], v[16:17], 0, s[46:47]
	global_load_dword v107, v[16:17], off nt
	v_lshl_add_u64 v[16:17], v[16:17], 0, s[46:47]
	global_load_dword v117, v[16:17], off nt
	v_lshl_add_u64 v[16:17], v[16:17], 0, s[46:47]
	global_load_dword v108, v[16:17], off nt
	v_lshl_add_u64 v[16:17], v[16:17], 0, s[46:47]
	global_load_dword v118, v[16:17], off nt
	v_lshl_add_u64 v[16:17], v[16:17], 0, s[46:47]
	global_load_dword v109, v[16:17], off nt
	v_lshl_add_u64 v[16:17], v[16:17], 0, s[46:47]
	global_load_dword v119, v[16:17], off nt
	v_lshl_add_u64 v[16:17], v[16:17], 0, s[46:47]
	global_load_dword v110, v[16:17], off nt
	v_lshl_add_u64 v[16:17], v[16:17], 0, s[46:47]
	global_load_dword v120, v[16:17], off nt
	v_lshl_add_u64 v[16:17], v[16:17], 0, s[46:47]
	global_load_dword v111, v[16:17], off nt
	v_lshl_add_u64 v[16:17], v[16:17], 0, s[46:47]
	global_load_dword v121, v[16:17], off nt
	v_lshl_add_u64 v[16:17], v[16:17], 0, s[46:47]
	global_load_dword v112, v[16:17], off nt
	v_lshl_add_u64 v[16:17], v[16:17], 0, s[46:47]
	global_load_dword v122, v[16:17], off nt
	v_lshl_add_u64 v[16:17], v[16:17], 0, s[46:47]
	global_load_dword v102, v[16:17], off nt
	v_lshl_add_u64 v[16:17], v[16:17], 0, s[46:47]
	global_load_dword v103, v[16:17], off nt
	v_lshl_add_u64 v[16:17], v[16:17], 0, s[46:47]
	global_load_dword v113, v[16:17], off nt
	v_lshl_add_u64 v[16:17], v[16:17], 0, s[46:47]
	global_load_dword v123, v[16:17], off nt
	v_lshl_add_u64 v[16:17], v[16:17], 0, s[46:47]
	global_load_dword v125, v[16:17], off nt
	v_lshl_add_u64 v[16:17], v[16:17], 0, s[46:47]
	global_load_dword v126, v[16:17], off nt
	v_lshl_add_u64 v[16:17], v[16:17], 0, s[46:47]
	global_load_dword v127, v[16:17], off nt
	v_lshl_add_u64 v[16:17], v[16:17], 0, s[46:47]
	global_load_dword v128, v[16:17], off nt
	v_lshl_add_u64 v[16:17], v[16:17], 0, s[46:47]
	global_load_dword v129, v[16:17], off nt
	v_lshl_add_u64 v[16:17], v[16:17], 0, s[46:47]
	global_load_dword v130, v[16:17], off nt
	v_lshl_add_u64 v[16:17], v[16:17], 0, s[46:47]
	global_load_dword v131, v[16:17], off nt
	v_lshl_add_u64 v[16:17], v[16:17], 0, s[46:47]
	global_load_dword v132, v[16:17], off nt
	v_lshl_add_u64 v[16:17], v[16:17], 0, s[46:47]
	global_load_dword v133, v[16:17], off nt
	v_lshl_add_u64 v[16:17], v[16:17], 0, s[46:47]
	global_load_dword v134, v[16:17], off nt
	v_lshl_add_u64 v[16:17], v[16:17], 0, s[46:47]
	global_load_dword v135, v[16:17], off nt
	v_lshl_add_u64 v[16:17], v[16:17], 0, s[46:47]
	global_load_dword v136, v[16:17], off nt
	v_lshl_add_u64 v[16:17], v[16:17], 0, s[46:47]
	global_load_dword v137, v[16:17], off nt
	v_lshl_add_u64 v[16:17], v[16:17], 0, s[46:47]
	global_load_dword v138, v[16:17], off nt
	v_lshl_add_u64 v[16:17], v[16:17], 0, s[46:47]
	global_load_dword v139, v[16:17], off nt
	v_lshl_add_u64 v[16:17], v[16:17], 0, s[46:47]
	global_load_dword v140, v[16:17], off nt
	v_lshl_add_u64 v[16:17], v[16:17], 0, s[46:47]
	global_load_dword v141, v[16:17], off nt
	v_lshl_add_u64 v[16:17], v[16:17], 0, s[46:47]
	global_load_dword v142, v[16:17], off nt
	v_lshl_add_u64 v[16:17], v[16:17], 0, s[46:47]
	global_load_dword v143, v[16:17], off nt
	v_lshl_add_u64 v[16:17], v[16:17], 0, s[46:47]
	global_load_dword v144, v[16:17], off nt
	v_lshl_add_u64 v[16:17], v[16:17], 0, s[46:47]
	global_load_dword v146, v[16:17], off nt
	v_lshl_add_u64 v[16:17], v[16:17], 0, s[46:47]
	global_load_dword v147, v[16:17], off nt
	v_lshl_add_u64 v[16:17], v[16:17], 0, s[46:47]
	global_load_dword v148, v[16:17], off nt
	v_lshl_add_u64 v[16:17], v[16:17], 0, s[46:47]
	global_load_dword v149, v[16:17], off nt
	v_lshl_add_u64 v[16:17], v[16:17], 0, s[46:47]
	global_load_dword v151, v[16:17], off nt
	v_lshl_add_u64 v[16:17], v[16:17], 0, s[46:47]
	global_load_dword v152, v[16:17], off nt
	v_lshl_add_u64 v[16:17], v[16:17], 0, s[46:47]
	global_load_dword v153, v[16:17], off nt
	v_lshl_add_u64 v[16:17], v[16:17], 0, s[46:47]
	global_load_dword v154, v[16:17], off nt
	v_lshl_add_u64 v[16:17], v[16:17], 0, s[46:47]
	global_load_dword v155, v[16:17], off nt
	v_lshl_add_u64 v[16:17], v[16:17], 0, s[46:47]
	global_load_dword v157, v[16:17], off nt
	v_lshl_add_u64 v[16:17], v[16:17], 0, s[46:47]
	global_load_dword v158, v[16:17], off nt
	v_lshl_add_u64 v[16:17], v[16:17], 0, s[46:47]
	ds_write2st64_b32 v28, v91, v90 offset0:2 offset1:3
	ds_write2st64_b32 v28, v89, v88 offset0:4 offset1:5
	ds_write2st64_b32 v28, v86, v85 offset0:6 offset1:7
	ds_write2st64_b32 v21, v83, v84 offset0:8 offset1:9
	ds_write2st64_b32 v21, v79, v80 offset0:10 offset1:11
	ds_write2st64_b32 v21, v75, v76 offset0:12 offset1:13
	ds_write2st64_b32 v21, v71, v72 offset0:14 offset1:15
	ds_write2st64_b32 v22, v65, v66 offset0:16 offset1:17
	ds_write2st64_b32 v22, v61, v62 offset0:18 offset1:19
	ds_write2st64_b32 v22, v57, v58 offset0:20 offset1:21
	ds_write2st64_b32 v22, v53, v54 offset0:22 offset1:23
	ds_write2st64_b32 v23, v45, v46 offset0:24 offset1:25
	ds_write2st64_b32 v23, v35, v36 offset0:26 offset1:27
	ds_write2st64_b32 v23, v33, v34 offset0:28 offset1:29
	ds_write2st64_b32 v23, v31, v32 offset0:30 offset1:31
	ds_write2st64_b32 v24, v29, v30 offset0:32 offset1:33
	ds_write2st64_b32 v24, v81, v82 offset0:34 offset1:35
	ds_write2st64_b32 v24, v77, v78 offset0:36 offset1:37
	ds_write2st64_b32 v24, v73, v74 offset0:38 offset1:39
	ds_write2st64_b32 v25, v69, v70 offset0:40 offset1:41
	ds_write2st64_b32 v25, v67, v68 offset0:42 offset1:43
	ds_write2st64_b32 v25, v63, v64 offset0:44 offset1:45
	ds_write2st64_b32 v25, v59, v60 offset0:46 offset1:47
	ds_write2st64_b32 v26, v55, v56 offset0:48 offset1:49
	ds_write2st64_b32 v26, v51, v52 offset0:50 offset1:51
	global_load_dword v159, v[16:17], off nt
	ds_write2st64_b32 v26, v38, v39 offset0:52 offset1:53
	ds_write2st64_b32 v26, v40, v42 offset0:54 offset1:55
	ds_write2st64_b32 v27, v37, v41 offset0:56 offset1:57
	ds_write2st64_b32 v27, v43, v44 offset0:58 offset1:59
	ds_write2st64_b32 v27, v47, v48 offset0:60 offset1:61
	ds_write2st64_b32 v27, v49, v50 offset0:62 offset1:63
	s_waitcnt lgkmcnt(0)
	ds_read2_b32 v[16:17], v1 offset1:32
	v_mov_b32_e32 v30, 0
	ds_read2_b32 v[32:33], v1 offset0:128 offset1:160
	v_mov_b32_e32 v31, 0
	v_add_u32_e32 v145, 0x400, v1
	s_waitcnt lgkmcnt(1)
	v_mul_f32_e32 v4, 0x42800000, v16
	v_mul_f32_e32 v15, 0x42800000, v17
	ds_read2_b32 v[16:17], v1 offset0:64 offset1:96
	v_cvt_pk_fp8_f32 v30, v4, v15
	ds_read2_b32 v[34:35], v145 offset0:128 offset1:160
	v_add_u32_e32 v150, 0x400, v9
	ds_read2_b32 v[38:39], v150 offset0:128 offset1:160
	s_waitcnt lgkmcnt(2)
	v_mul_f32_e32 v4, 0x42800000, v16
	v_mul_f32_e32 v15, 0x42800000, v17
	ds_read2_b32 v[16:17], v1 offset0:192 offset1:224
	v_cvt_pk_fp8_f32 v30, v4, v15 op_sel:[0,0,1]
	v_mul_f32_e32 v4, 0x42800000, v32
	v_mul_f32_e32 v15, 0x42800000, v33
	v_cvt_pk_fp8_f32 v31, v4, v15
	s_waitcnt lgkmcnt(0)
	v_mul_f32_e32 v4, 0x42800000, v16
	v_mul_f32_e32 v15, 0x42800000, v17
	ds_read2_b32 v[16:17], v145 offset0:64 offset1:96
	ds_read2_b32 v[32:33], v145 offset1:32
	v_cvt_pk_fp8_f32 v31, v4, v15 op_sel:[0,0,1]
	v_lshl_add_u64 v[10:11], v[10:11], 0, v[6:7]
	v_add_u32_e32 v156, 0x400, v18
	s_waitcnt lgkmcnt(1)
	v_mul_f32_e32 v29, 0x42800000, v16
	v_mul_f32_e32 v36, 0x42800000, v17
	ds_read2_b32 v[16:17], v145 offset0:192 offset1:224
	s_waitcnt lgkmcnt(1)
	v_mul_f32_e32 v4, 0x42800000, v32
	v_mul_f32_e32 v15, 0x42800000, v33
	v_mov_b32_e32 v32, 0
	v_cvt_pk_fp8_f32 v32, v4, v15
	v_mul_f32_e32 v4, 0x42800000, v34
	v_mul_f32_e32 v15, 0x42800000, v35
	v_mov_b32_e32 v33, 0
	ds_read2_b32 v[34:35], v9 offset1:32
	v_cvt_pk_fp8_f32 v33, v4, v15
	s_waitcnt lgkmcnt(1)
	v_mul_f32_e32 v4, 0x42800000, v16
	v_mul_f32_e32 v15, 0x42800000, v17
	ds_read2_b32 v[16:17], v9 offset0:64 offset1:96
	v_cvt_pk_fp8_f32 v32, v29, v36 op_sel:[0,0,1]
	ds_read2_b32 v[36:37], v9 offset0:128 offset1:160
	v_cvt_pk_fp8_f32 v33, v4, v15 op_sel:[0,0,1]
	s_waitcnt lgkmcnt(2)
	v_mul_f32_e32 v4, 0x42800000, v34
	v_mul_f32_e32 v15, 0x42800000, v35
	v_mov_b32_e32 v34, 0
	v_cvt_pk_fp8_f32 v34, v4, v15
	s_waitcnt lgkmcnt(1)
	v_mul_f32_e32 v4, 0x42800000, v16
	v_mul_f32_e32 v15, 0x42800000, v17
	ds_read2_b32 v[16:17], v9 offset0:192 offset1:224
	s_waitcnt lgkmcnt(1)
	v_mul_f32_e32 v29, 0x42800000, v36
	v_mul_f32_e32 v36, 0x42800000, v37
	v_mov_b32_e32 v35, 0
	v_cvt_pk_fp8_f32 v35, v29, v36
	ds_read2_b32 v[36:37], v150 offset1:32
	v_cvt_pk_fp8_f32 v34, v4, v15 op_sel:[0,0,1]
	s_waitcnt lgkmcnt(1)
	v_mul_f32_e32 v4, 0x42800000, v16
	v_mul_f32_e32 v15, 0x42800000, v17
	ds_read2_b32 v[16:17], v150 offset0:64 offset1:96
	v_cvt_pk_fp8_f32 v35, v4, v15 op_sel:[0,0,1]
	s_waitcnt lgkmcnt(1)
	v_mul_f32_e32 v4, 0x42800000, v36
	v_mul_f32_e32 v15, 0x42800000, v37
	v_mov_b32_e32 v36, 0
	v_cvt_pk_fp8_f32 v36, v4, v15
	s_waitcnt lgkmcnt(0)
	v_mul_f32_e32 v4, 0x42800000, v16
	v_mul_f32_e32 v15, 0x42800000, v17
	ds_read2_b32 v[16:17], v150 offset0:192 offset1:224
	v_cvt_pk_fp8_f32 v36, v4, v15 op_sel:[0,0,1]
	v_mul_f32_e32 v4, 0x42800000, v38
	v_mul_f32_e32 v15, 0x42800000, v39
	v_mov_b32_e32 v37, 0
	v_cvt_pk_fp8_f32 v37, v4, v15
	s_waitcnt lgkmcnt(0)
	v_mul_f32_e32 v4, 0x42800000, v16
	v_mul_f32_e32 v15, 0x42800000, v17
	ds_read2_b32 v[16:17], v18 offset1:32
	v_cvt_pk_fp8_f32 v37, v4, v15 op_sel:[0,0,1]
	global_store_dwordx4 v[10:11], v[30:33], off sc0 sc1 nt
	ds_read2_b32 v[32:33], v18 offset0:64 offset1:96
	s_lshl_b64 s[38:39], s[38:39], 3
	s_waitcnt lgkmcnt(1)
	v_mul_f32_e32 v4, 0x42800000, v16
	v_mul_f32_e32 v15, 0x42800000, v17
	ds_read2_b32 v[16:17], v18 offset0:128 offset1:160
	v_mov_b32_e32 v30, 0
	v_cvt_pk_fp8_f32 v30, v4, v15
	s_waitcnt lgkmcnt(1)
; __device__ __forceinline__ MoeItem moe_item(const float* wg, const float* wu, const float* wd, const float* win, const float* wout, const float* wpn, const float* wpd, unsigned char* ws, int r, int lane) {
;     if (r >= NMOE_X + NGATE_IT + NWO_IT) { const int q = r - NMOE_X - NGATE_IT - NWO_IT, which = q >> 9, kb = (q >> 6) & 7, nb = q & 63; MoeItem it; it.stride = DM; it.dpitch = 1024;
;         it.src = (which ? wpd : wpn) + (size_t)(kb * 128 + (lane >> 5)) * DM + nb * 32 + (lane & 31);
;         it.dst = ws + (which ? WS_WPDFT : WS_WPNAT) + (size_t)(nb * 32) * 1024 + kb * 128 + (size_t)(lane >> 3) * 1024 + 16 * (lane & 7); return it; }
;     if (r >= NMOE_X + NGATE_IT) { const int q = r - NMOE_X - NGATE_IT, kb = q >> 6, nb = q & 63; MoeItem it; it.stride = DM; it.dpitch = DM;
;         it.src = wout + (size_t)(kb * 128 + (lane >> 5)) * DM + nb * 32 + (lane & 31);
;         it.dst = ws + WS_WO8 + (size_t)(nb * 32) * DM + kb * 128 + (size_t)(lane >> 3) * DM + 16 * (lane & 7); return it; }
;     if (r >= NMOE_X) { const int q = r - NMOE_X, kb = q / 192, nb = q % 192; MoeItem it; it.stride = INC; it.dpitch = DM;
;         const int scol = nb < 128 ? 6144 + nb * 32 : (nb < 160 ? 1024 + (nb - 128) * 32 : 3072 + (nb - 160) * 32);
;         it.src = win + (size_t)(kb * 128 + (lane >> 5)) * INC + scol + (lane & 31);
;         it.dst = ws + WS_WG8 + (size_t)(nb * 32) * DM + kb * 128 + (size_t)(lane >> 3) * DM + 16 * (lane & 7); return it; }
;     const int mat = r / MOE_IE, q = r % MOE_IE, e = mat / 3, which = mat % 3, kb = q / 64, nb = q % 64, n0 = nb * 32;
;     const float* src = (which == 0 ? wg : (which == 1 ? wu : wd)) + (size_t)e * DM * DFF + (size_t)(kb * 128 + (lane >> 5)) * DFF + n0 + (lane & 31);
;     unsigned char* dst;
;     if (which < 2) dst = ws + WS_WGUT + ((size_t)(e * 16 + (n0 >> 7)) * 256 + which * 128 + (n0 & 127)) * DM;
;     else dst = ws + WS_WDT + ((size_t)e * DM + n0) * DFF;
;     MoeItem it; it.stride = DFF; it.dpitch = DM; it.src = src; it.dst = dst + kb * 128 + (size_t)(lane >> 3) * DM + 16 * (lane & 7); return it;
	v_mul_f32_e32 v4, 0x42800000, v32
	v_mov_b32_e32 v31, 0
	s_waitcnt lgkmcnt(0)
	v_mul_f32_e32 v29, 0x42800000, v16
	v_mul_f32_e32 v32, 0x42800000, v17
	ds_read2_b32 v[16:17], v18 offset0:192 offset1:224
	v_mul_f32_e32 v15, 0x42800000, v33
	v_cvt_pk_fp8_f32 v31, v29, v32
	ds_read2_b32 v[32:33], v156 offset1:32
	v_cvt_pk_fp8_f32 v30, v4, v15 op_sel:[0,0,1]
	s_waitcnt lgkmcnt(1)
	v_mul_f32_e32 v4, 0x42800000, v16
	v_mul_f32_e32 v15, 0x42800000, v17
	ds_read2_b32 v[16:17], v156 offset0:64 offset1:96
	v_lshl_add_u64 v[10:11], v[10:11], 0, s[38:39]
	global_store_dwordx4 v[10:11], v[34:37], off sc0 sc1 nt
	ds_read2_b32 v[34:35], v156 offset0:128 offset1:160
	v_cvt_pk_fp8_f32 v31, v4, v15 op_sel:[0,0,1]
	s_waitcnt lgkmcnt(2)
	v_mul_f32_e32 v4, 0x42800000, v32
	v_mul_f32_e32 v15, 0x42800000, v33
	v_mov_b32_e32 v32, 0
	v_cvt_pk_fp8_f32 v32, v4, v15
	s_waitcnt lgkmcnt(1)
	v_mul_f32_e32 v4, 0x42800000, v16
	v_mul_f32_e32 v15, 0x42800000, v17
	ds_read2_b32 v[16:17], v156 offset0:192 offset1:224
	s_waitcnt lgkmcnt(1)
	v_mul_f32_e32 v29, 0x42800000, v34
	v_mul_f32_e32 v34, 0x42800000, v35
	v_mov_b32_e32 v33, 0
	v_cvt_pk_fp8_f32 v33, v29, v34
	ds_read2_b32 v[34:35], v19 offset1:32
	v_cvt_pk_fp8_f32 v32, v4, v15 op_sel:[0,0,1]
	s_waitcnt lgkmcnt(1)
	v_mul_f32_e32 v4, 0x42800000, v16
	v_mul_f32_e32 v15, 0x42800000, v17
	ds_read2_b32 v[16:17], v19 offset0:64 offset1:96
	ds_read2_b32 v[36:37], v19 offset0:128 offset1:160
	v_cvt_pk_fp8_f32 v33, v4, v15 op_sel:[0,0,1]
	s_waitcnt lgkmcnt(2)
	v_mul_f32_e32 v4, 0x42800000, v34
	v_mul_f32_e32 v15, 0x42800000, v35
	v_mov_b32_e32 v34, 0
	v_cvt_pk_fp8_f32 v34, v4, v15
	s_waitcnt lgkmcnt(1)
	v_mul_f32_e32 v4, 0x42800000, v16
	v_mul_f32_e32 v15, 0x42800000, v17
	ds_read2_b32 v[16:17], v19 offset0:192 offset1:224
	s_waitcnt lgkmcnt(1)
	v_mul_f32_e32 v29, 0x42800000, v36
	v_mul_f32_e32 v36, 0x42800000, v37
	v_mov_b32_e32 v35, 0
	v_add_u32_e32 v160, 0x400, v19
	v_cvt_pk_fp8_f32 v35, v29, v36
	ds_read2_b32 v[36:37], v160 offset1:32
	v_cvt_pk_fp8_f32 v34, v4, v15 op_sel:[0,0,1]
	s_waitcnt lgkmcnt(1)
	v_mul_f32_e32 v4, 0x42800000, v16
	v_mul_f32_e32 v15, 0x42800000, v17
	ds_read2_b32 v[16:17], v160 offset0:64 offset1:96
	ds_read2_b32 v[38:39], v160 offset0:128 offset1:160
	v_cvt_pk_fp8_f32 v35, v4, v15 op_sel:[0,0,1]
	s_waitcnt lgkmcnt(2)
	v_mul_f32_e32 v4, 0x42800000, v36
	v_mul_f32_e32 v15, 0x42800000, v37
	v_mov_b32_e32 v36, 0
	v_cvt_pk_fp8_f32 v36, v4, v15
	s_waitcnt lgkmcnt(1)
	v_mul_f32_e32 v4, 0x42800000, v16
	v_mul_f32_e32 v15, 0x42800000, v17
	ds_read2_b32 v[16:17], v160 offset0:192 offset1:224
	s_waitcnt lgkmcnt(1)
	v_mul_f32_e32 v29, 0x42800000, v38
	v_mul_f32_e32 v38, 0x42800000, v39
	v_mov_b32_e32 v37, 0
	v_cvt_pk_fp8_f32 v37, v29, v38
	v_cvt_pk_fp8_f32 v36, v4, v15 op_sel:[0,0,1]
	s_waitcnt lgkmcnt(0)
	v_mul_f32_e32 v4, 0x42800000, v16
	v_mul_f32_e32 v15, 0x42800000, v17
	v_cvt_pk_fp8_f32 v37, v4, v15 op_sel:[0,0,1]
	v_lshl_add_u64 v[10:11], v[10:11], 0, s[38:39]
	global_store_dwordx4 v[10:11], v[30:33], off sc0 sc1 nt
	v_lshl_add_u64 v[10:11], v[10:11], 0, s[38:39]
	global_store_dwordx4 v[10:11], v[34:37], off sc0 sc1 nt
	s_waitcnt lgkmcnt(0)
	s_add_i32 s3, s89, s3
	s_mov_b32 s96, 0
	s_min_i32 s43, s3, s7
	s_cmp_lt_i32 s43, 0x19000
	s_mov_b64 s[38:39], -1
	s_cbranch_scc0 .LBB0_126
	s_cmp_lt_i32 s43, 0x18c00
	s_cbranch_scc0 .LBB0_123
	s_cmp_lt_i32 s43, 0x18000
	s_cbranch_scc0 .LBB0_113
	s_mov_b32 s96, 1
	s_ashr_i32 s4, s43, 31
	s_lshr_b32 s4, s4, 22
	s_add_i32 s4, s43, s4
	s_ashr_i32 s39, s4, 10
	s_and_b32 s4, s4, 0xfc00
	s_sub_i32 s46, s43, s4
	s_mul_hi_i32 s4, s43, 0x2aaaaaab
	s_lshr_b32 s38, s4, 31
	s_ashr_i32 s4, s4, 9
	s_add_i32 s38, s4, s38
	s_mul_hi_i32 s4, s39, 0x55555556
	s_lshr_b32 s45, s4, 31
	s_add_i32 s4, s4, s45
	s_mul_i32 s4, s4, 3
	s_sub_i32 s4, s39, s4
	s_sext_i32_i16 s39, s46
	s_bfe_u32 s39, s39, 0x60019
	s_add_i32 s45, s46, s39
	s_and_b32 s39, s45, 0xffc0
	s_sub_i32 s39, s46, s39
	s_sext_i32_i16 s84, s39
	s_lshl_b32 s46, s84, 5
	s_ashr_i32 s39, s38, 31
	s_ashr_i32 s47, s46, 31
	s_cmp_gt_i32 s4, 1
	s_mov_b64 s[70:71], -1
	s_cbranch_scc0 .LBB0_110
	s_mov_b32 s99, 16
	s_lshl_b64 s[68:69], s[38:39], 18
	s_lshl_b64 s[70:71], s[46:47], 7
	s_add_u32 s68, s73, s68
	s_addc_u32 s69, s74, s69
	s_add_u32 s68, s68, s70
	s_addc_u32 s69, s69, s71
	s_mov_b64 s[70:71], 0
.LBB0_110:
	s_andn2_b64 vcc, exec, s[70:71]
	s_cbranch_vccnz .LBB0_112
	s_lshl_b32 s68, s38, 4
	s_ashr_i32 s69, s84, 2
	s_add_i32 s68, s69, s68
	s_ashr_i32 s69, s68, 31
	s_lshl_b32 s70, s4, 7
	s_lshl_b64 s[68:69], s[68:69], 8
	s_ashr_i32 s71, s70, 31
	s_add_u32 s68, s68, s70
	s_addc_u32 s69, s69, s71
	s_and_b32 s70, s46, 0x60
	s_or_b32 s68, s68, s70
	s_mov_b32 s99, 17
	s_lshl_b64 s[68:69], s[68:69], 7
	s_add_u32 s68, s75, s68
	s_addc_u32 s69, s76, s69
.LBB0_112:
	s_sext_i32_i16 s45, s45
	s_lshr_b32 s45, s45, 6
	s_cmp_eq_u32 s4, 1
	s_cselect_b32 s70, s20, s24
	s_cselect_b32 s71, s21, s25
	s_cmp_eq_u32 s4, 0
	s_cselect_b32 s4, s17, s71
	s_cselect_b32 s70, s16, s70
	s_lshl_b64 s[38:39], s[38:39], 24
	s_sext_i32_i16 s45, s45
	s_add_u32 s38, s70, s38
	s_addc_u32 s39, s4, s39
	s_lshl_b32 s4, s45, 7
	v_or_b32_e32 v10, s4, v20
	v_ashrrev_i32_e32 v11, 31, v10
	v_lshlrev_b64 v[10:11], 13, v[10:11]
	v_lshl_add_u64 v[10:11], s[38:39], 0, v[10:11]
	s_ashr_i32 s38, s4, 31
	v_lshl_add_u64 v[10:11], s[46:47], 2, v[10:11]
	s_lshl_b32 s98, s4, s99
	s_add_u32 s46, s68, s98
	v_mov_b32_e32 v15, v5
	s_addc_u32 s47, s69, s38
	v_lshl_add_u64 v[16:17], v[10:11], 0, v[14:15]
	s_mov_b64 s[38:39], 0
	v_mov_b64_e32 v[10:11], s[46:47]

; #define PG8_WAIT_V(n) asm volatile("s_waitcnt vmcnt(" #n ")" ::: "memory")
; #define PG8_BAR __builtin_amdgcn_s_barrier()
; template <class Epi, class Sched, bool GATHER, bool F8 = false>
; __device__ __forceinline__ void gemm_phase(LAS unsigned char* lds, const int K, const Sched& S, const Epi& E) {
;     ...
;     Unit cur, nxt; int ui = 0;
;     if (!S.next(0, cur)) return;
;     if constexpr (GATHER) { S.offsets(0, RA, CA, vA); }
; #pragma unroll
;     for (int h = 0; h < 2; ++h)
; #pragma unroll
;         for (int i = 0; i < 2; ++i) vN[h][i] = vA[h][i];
;     f32x4 acc[2][2][4][2];
; #pragma unroll
;     for (int a = 0; a < 2; ++a)
; #pragma unroll
;         for (int b = 0; b < 2; ++b)
; #pragma unroll
;             for (int m = 0; m < 4; ++m)
; #pragma unroll
;                 for (int n = 0; n < 2; ++n) acc[a][b][m][n] = (f32x4){0.f, 0.f, 0.f, 0.f};
;     if constexpr (EpiInit<Epi>::value) { const typename EpiInit<Epi>::Pre p0 = E.preload(cur, wr, wc, fr, fq); E.init(acc, p0); }
;     int one_scale = 0x7f7f7f7f; asm volatile("" : "+v"(one_scale));
;     bf16x8 At[4][2], B0[2][2], B1[2][2]; i32x8 At8[4], B08[2], B18[2];
;     const char* cA = cur.A; const char* cB = cur.B;
;     PG8_STAGE(PG8_SB(0, 0), cB, voffB); PG8_STAGE(PG8_SB(0, 1), cB + hstepB, voffB); PG8_STAGE(PG8_SA(0, 0), cA, vA[0]); PG8_STAGE(PG8_SA(0, 1), cA, vA[1]);
;     if (wr == 1) PG8_BAR;
;     PG8_WAIT_V(2); PG8_BAR;
;     PG8_STAGE(PG8_SB(1, 0), cB + kstep, voffB); PG8_STAGE(PG8_SA(1, 0), cA + kstep, vA[0]); PG8_STAGE(PG8_SB(1, 1), cB + hstepB + kstep, voffB);
;     PG8_WAIT_V(6); PG8_BAR;
;     __device__ __forceinline__ bool next(int i, Unit& u) const {
;         const int x = c & 7, j = c >> 3, tile = 16 * i + 4 * (x >> 1) + (j & 3), nb = 8 * (x & 1) + (j >> 2);
;         if (tile >= tb.ntiles) return false;
;         const int e = tb.tile_e[tile];
;         u.A = U2; u.B = W + ((size_t)(e * 16 + nb) * 256) * DM; u.row0 = tile * 256; u.col0 = nb * 128; u.tag = e; u.aux = i; return true;
;     }
;     __device__ __forceinline__ void offsets(int i, const int (&RA)[2], const int (&CA)[2], unsigned (&v)[2][2]) const {
; #pragma unroll
;         for (int h = 0; h < 2; ++h)
; #pragma unroll
;             for (int k = 0; k < 2; ++k) { const int tok = tb.tokl[i * 256 + RA[k] + 128 * h]; v[h][k] = (unsigned)(tok * (DM / 2) + CA[k]) * 2u; }
;     }
.LBB0_1027:
	s_or_b64 exec, exec, s[10:11]
	v_and_b32_e32 v2, 0x100, v0
	v_mov_b32_e32 v5, 2
	s_add_i32 s0, 0, 0x20000
	v_lshlrev_b32_e32 v2, 2, v2
	v_lshlrev_b32_sdwa v5, v5, v0 dst_sel:DWORD dst_unused:UNUSED_PAD src0_sel:DWORD src1_sel:BYTE_0
	s_or_b32 s6, s6, s7
	v_add3_u32 v2, s0, v2, v5
	s_cmp_ge_i32 s6, s3
	v_readfirstlane_b32 s20, v0
	s_waitcnt vmcnt(0)
	ds_write2st64_b32 v2, v4, v1 offset0:8 offset1:16
	ds_write2st64_b32 v2, v7, v6 offset0:24 offset1:32
	ds_write_b32 v2, v3 offset:10240
	s_waitcnt lgkmcnt(0)
	s_barrier
	s_cbranch_scc1 .LBB0_1045
	v_lshlrev_b32_e32 v1, 4, v0
	v_and_b32_e32 v2, 32, v0
	v_bfe_u32 v4, v0, 3, 25
	s_add_u32 s7, s82, 0x4000000
	v_bfe_u32 v3, v0, 2, 4
	v_bitop3_b32 v1, v1, v2, 48 bitop3:0x6c
	v_lshrrev_b32_e32 v2, 3, v0
	v_or_b32_e32 v4, 64, v4
	s_movk_i32 s0, 0x70
	s_addc_u32 s25, s83, 0
	v_and_or_b32 v160, v2, 48, v3
	v_and_or_b32 v161, v4, s0, v3
	s_lshl_b32 s0, s20, 4
	v_lshrrev_b32_e32 v3, 1, v0
	s_and_b32 s37, s0, 0xfffffc00
	v_and_b32_e32 v14, 24, v3
	s_lshr_b32 s0, s20, 1
	v_lshrrev_b32_e32 v3, 5, v0
	s_lshr_b32 s21, s20, 8
	s_and_b32 s14, s0, 0x60
	v_and_b32_e32 v3, 4, v3
	v_bfe_u32 v5, v0, 2, 2
	s_movk_i32 s10, 0x60
	s_add_u32 s0, s82, 0x2c000000
	v_or3_b32 v3, v3, v5, v14
	s_addc_u32 s1, s83, 0
	v_and_or_b32 v4, v4, s10, v3
	s_lshl_b32 s10, s6, 2
	s_add_i32 s10, s10, 0
	v_and_or_b32 v1, v0, 64, v1
	v_and_or_b32 v2, v2, 32, v3
	s_add_i32 s10, s10, 0x20000
	v_lshl_or_b32 v148, v2, 11, v1
	v_mov_b32_e32 v2, s10
	ds_read_b32 v150, v2
	s_lshl_b32 s10, s2, 3
	s_and_b32 s39, s10, 8
	s_ashr_i32 s10, s2, 5
	s_add_i32 s39, s39, s10
	s_waitcnt lgkmcnt(0)
	v_readfirstlane_b32 s10, v150
	s_lshl_b32 s10, s10, 4
	s_add_i32 s10, s10, s39
	s_ashr_i32 s11, s10, 31
	s_lshl_b64 s[10:11], s[10:11], 15
	s_add_u32 s44, s7, s10
	v_lshl_or_b32 v146, v4, 11, v1
	v_lshrrev_b32_e32 v254, 11, v148
	v_and_b32_e32 v148, 0x7f, v148
	v_lshl_or_b32 v148, v254, 7, v148
	v_lshrrev_b32_e32 v254, 11, v146
	v_and_b32_e32 v146, 0x7f, v146
	v_lshl_or_b32 v146, v254, 7, v146
	s_addc_u32 s45, s25, s11
	s_add_i32 s10, 0, 0x20800
	v_lshlrev_b32_e32 v2, 2, v160
	v_lshlrev_b32_e32 v4, 2, v161
	v_add_u32_e32 v3, s10, v2
	v_add_u32_e32 v5, s10, v4
	s_add_i32 s10, 0, 0x20a00
	v_add_u32_e32 v2, s10, v2
	v_add_u32_e32 v4, s10, v4
	ds_read_b32 v3, v3
	ds_read_b32 v5, v5
	ds_read_b32 v2, v2
	ds_read_b32 v4, v4
	s_lshl_b32 s50, s39, 7
	v_or_b32_e32 v162, s14, v14
	v_ashrrev_i32_e32 v151, 31, v150
	s_waitcnt lgkmcnt(1)
	v_lshl_or_b32 v163, v2, 11, v1
	v_or_b32_e32 v2, s50, v162
	v_lshl_or_b32 v152, v3, 11, v1
	v_lshl_or_b32 v154, v5, 11, v1
	s_waitcnt lgkmcnt(0)
	v_lshl_or_b32 v164, v4, 11, v1
	v_lshlrev_b64 v[4:5], 13, v[150:151]
	v_ashrrev_i32_e32 v3, 31, v2
	v_lshl_add_u64 v[6:7], s[18:19], 0, v[4:5]
	v_lshlrev_b64 v[2:3], 2, v[2:3]
	s_add_i32 s51, s37, 0
	v_lshl_add_u64 v[10:11], v[6:7], 0, v[2:3]
	v_lshl_add_u64 v[4:5], s[22:23], 0, v[4:5]
	v_mov_b32_e32 v165, 0x7f7f7f7f
	s_add_i32 m0, s51, 0x10000
	v_lshl_add_u64 v[12:13], v[4:5], 0, v[2:3]
	global_load_dwordx4 v[58:61], v[10:11], off offset:16
	global_load_dwordx4 v[62:65], v[10:11], off
	global_load_dwordx4 v[2:5], v[12:13], off offset:16
	global_load_dwordx4 v[6:9], v[12:13], off
	global_load_lds_dwordx4 v148, s[44:45]
	s_add_i32 m0, s51, 0x12000
	s_add_u32 s10, s44, 0x4000
	global_load_lds_dwordx4 v146, s[44:45]
	s_addc_u32 s11, s45, 0
	s_add_i32 m0, s51, 0x14000
	s_add_i32 s52, s51, 0x2000
	global_load_lds_dwordx4 v148, s[10:11]
	s_add_i32 m0, s51, 0x16000
	s_add_i32 s53, s51, 0x4000
	global_load_lds_dwordx4 v146, s[10:11]
	s_mov_b32 m0, s51
	s_add_i32 s54, s51, 0x6000
	global_load_lds_dwordx4 v152, s[0:1]
	s_mov_b32 m0, s52
	v_mov_b32_e32 v153, 0
	global_load_lds_dwordx4 v154, s[0:1]
	s_mov_b32 m0, s53
	v_mov_b32_e32 v149, v153
	global_load_lds_dwordx4 v163, s[0:1]
	s_mov_b32 m0, s54
	v_mov_b32_e32 v147, v153
	global_load_lds_dwordx4 v164, s[0:1]
	s_cmp_eq_u32 s21, 1
	v_lshl_add_u64 v[12:13], s[44:45], 0, v[148:149]
	v_lshl_add_u64 v[10:11], s[44:45], 0, v[146:147]
	s_cselect_b64 s[10:11], -1, 0
	s_cmp_lg_u32 s21, 1
	v_mov_b32_e32 v155, v153
	s_cbranch_scc1 .LBB0_1030
	s_barrier
.LBB0_1030:
	s_lshl_b32 s64, s6, 8
	s_add_u32 s12, s82, 0x34000000
	s_addc_u32 s13, s83, 0
	s_lshl_b32 s36, s14, 7
	s_mov_b64 s[14:15], 0x80
	s_mov_b64 s[100:101], 0x1000000
	s_add_i32 m0, s51, 0x18000
	v_lshl_add_u64 v[12:13], v[12:13], 0, s[100:101]
	s_lshl_b32 s24, s21, 13
	s_waitcnt vmcnt(2)
	s_barrier
	global_load_lds_dwordx4 v[12:13], off
	s_add_i32 m0, s51, 0x1a000
	s_add_u32 s16, s82, 0x2c000080
	v_lshl_add_u64 v[10:11], v[10:11], 0, s[100:101]
	s_addc_u32 s17, s83, 0
	s_add_i32 s55, s51, 0x8000
	s_add_i32 s56, s51, 0xa000
	global_load_lds_dwordx4 v[10:11], off
	v_lshl_add_u64 v[10:11], s[16:17], 0, v[152:153]
	s_mov_b32 m0, s55
	s_add_u32 s40, s44, 0x1004000
	global_load_lds_dwordx4 v[10:11], off
	v_lshl_add_u64 v[10:11], s[16:17], 0, v[154:155]
	s_mov_b32 m0, s56
	s_addc_u32 s41, s45, 0
	global_load_lds_dwordx4 v[10:11], off
	s_add_i32 m0, s51, 0x1c000
	v_lshl_add_u64 v[10:11], s[40:41], 0, v[148:149]
	global_load_lds_dwordx4 v[10:11], off
	v_lshl_add_u64 v[10:11], s[40:41], 0, v[146:147]
	s_add_i32 m0, s51, 0x1e000
	v_lshlrev_b32_e32 v12, 2, v0
	global_load_lds_dwordx4 v[10:11], off
	v_and_b32_e32 v10, 15, v0
	v_lshlrev_b32_e32 v11, 1, v14
	v_lshl_or_b32 v166, s21, 6, v10
	v_lshl_or_b32 v10, v10, 6, v11
	v_and_b32_e32 v12, 32, v12
	v_lshlrev_b32_e32 v13, 6, v0
	s_movk_i32 s21, 0x3c0
	s_waitcnt vmcnt(6)
	v_bitop3_b32 v10, v10, s24, v12 bitop3:0xde
	v_and_or_b32 v11, v13, s21, v11
	s_cmpk_lt_u32 s20, 0x100
	v_bitop3_b32 v167, s36, v11, v12 bitop3:0xf6
	s_mov_b32 s57, 0
	s_cselect_b64 s[20:21], -1, 0
	s_mov_b32 s24, 0x42800000
	s_add_i32 s58, 0, 0x10000
	s_add_i32 s59, 0, 0x14000
	v_add_u32_e32 v168, 0, v10
	s_mov_b32 s36, 0x3c800000
	s_mov_b32 s60, 0xc0c00000
	s_mov_b32 s38, 0xc01d265f
	s_add_i32 s61, s51, 0xc000
	s_add_i32 s62, s51, 0xe000
	v_mov_b32_e32 v169, 0x41000000
	s_mov_b64 s[40:41], s[44:45]
	s_barrier
	s_branch .LBB0_1033

; #define PG8_STAGE(bufoff, gbase, voff) do { _Pragma("unroll") for (int _i = 0; _i < 2; ++_i) \
;         __builtin_amdgcn_global_load_lds((const unsigned*)((const char*)(gbase) + (voff)[_i]), (LAS unsigned*)(lds + (bufoff) + ldsw + _i * 8192), 16, 0, 0); } while (0)
; #define PG8_LDA(dst, b, h) do { _Pragma("unroll") for (int m = 0; m < 4; ++m) { if constexpr (F8) dst##8[m] = PG8_LD32(lds + PG8_SA(b, h) + aoff + m * 2048); \
;         else { _Pragma("unroll") for (int k = 0; k < 2; ++k) dst[m][k] = *(const LAS bf16x8*)(lds + PG8_SA(b, h) + aoff + m * 2048 + k * 1024); } } } while (0)
; #define PG8_WAIT_V(n) asm volatile("s_waitcnt vmcnt(" #n ")" ::: "memory")
; #define PG8_BAR __builtin_amdgcn_s_barrier()
; template <class Epi, class Sched, bool GATHER, bool F8 = false>
; __device__ __forceinline__ void gemm_phase(LAS unsigned char* lds, const int K, const Sched& S, const Epi& E) {
;     ...
;     for (;;) {
;         const bool has_next = S.next(ui + 1, nxt);
;         const char* nA = has_next ? nxt.A : cA; const char* nB = has_next ? nxt.B : cB;
;         for (int t = 0; t < nt; t += 2) {
;             const bool last = (t == nt - 2);
;             const char* a1 = cA + (size_t)(t + 1) * kstep;
;             const char* a2 = last ? nA : cA + (size_t)(t + 2) * kstep; const char* b2 = last ? nB : cB + (size_t)(t + 2) * kstep;
;             const char* a3 = a2 + kstep; const char* b3 = b2 + kstep;
;             if constexpr (GATHER) { if (last && has_next) S.offsets(ui + 1, RA, CA, vN); }
;             PG8_LDB(B0, 0, 0); PG8_LDB(B1, 0, 1); PG8_SCHED; PG8_LDA(At, 0, 0); PG8_STAGE(PG8_SA(1, 1), a1, vA[1]);
;             PG8_WAIT_V(8); PG8_WAIT_L(0); PG8_BAR; PG8_MMA(0, 0, At, B0); PG8_MMA(0, 1, At, B1); PG8_BAR; PG8_SCHED;
;             PG8_LDA(At, 0, 1); PG8_STAGE(PG8_SB(0, 0), b2, voffB); PG8_STAGE(PG8_SB(0, 1), b2 + hstepB, voffB); PG8_STAGE(PG8_SA(0, 0), a2, vN[0]);
;             PG8_WAIT_V(8); PG8_WAIT_L(0); PG8_BAR; PG8_MMA(1, 0, At, B0); PG8_MMA(1, 1, At, B1); PG8_BAR; PG8_SCHED;
;     __device__ __forceinline__ void init(f32x4 (&acc)[2][2][4][2], const Pre& p) const {
; #pragma unroll
;         for (int ai = 0; ai < 2; ++ai)
; #pragma unroll
;             for (int m = 0; m < 4; ++m)
; #pragma unroll
;                 for (int n = 0; n < 2; ++n) { acc[ai][0][m][n] = p.g[n] * WSCALE; acc[ai][1][m][n] = (p.u[n] + 1.0f) * WSCALE; }
;     }
.LBB0_1033:
	s_add_i32 s57, s57, 1
	s_lshl_b32 s42, s57, 4
	s_or_b32 s46, s42, s6
	s_cmp_lt_i32 s46, s3
	s_cselect_b64 s[42:43], -1, 0
	s_cmp_ge_i32 s46, s3
	s_cbranch_scc1 .LBB0_1035
	s_lshl_b32 s40, s46, 2
	s_add_i32 s40, s40, 0
	s_add_i32 s40, s40, 0x20000
	v_mov_b32_e32 v10, s40
	ds_read_b32 v150, v10
	s_waitcnt lgkmcnt(0)
	v_readfirstlane_b32 s40, v150
	s_lshl_b32 s40, s40, 4
	s_add_i32 s40, s40, s39
	s_ashr_i32 s41, s40, 31
	s_lshl_b64 s[40:41], s[40:41], 15
	s_add_u32 s40, s7, s40
	s_addc_u32 s41, s25, s41
	s_lshl_b32 s63, s46, 8
.LBB0_1035:
	s_lshl_b32 s46, s57, 10
	s_waitcnt vmcnt(0)
	v_pk_add_f32 v[8:9], v[8:9], 1.0 op_sel_hi:[1,0]
	v_pk_add_f32 v[4:5], v[4:5], 1.0 op_sel_hi:[1,0]
	s_add_i32 s46, s46, 0
	v_pk_mul_f32 v[20:21], v[64:65], s[24:25] op_sel_hi:[1,0]
	v_pk_mul_f32 v[12:13], v[60:61], s[24:25] op_sel_hi:[1,0]
	v_pk_add_f32 v[6:7], v[6:7], 1.0 op_sel_hi:[1,0]
	v_pk_mul_f32 v[24:25], v[8:9], s[24:25] op_sel_hi:[1,0]
	v_pk_add_f32 v[2:3], v[2:3], 1.0 op_sel_hi:[1,0]
	v_pk_mul_f32 v[16:17], v[4:5], s[24:25] op_sel_hi:[1,0]
	s_add_i32 s46, s46, 0x20800
	v_pk_mul_f32 v[18:19], v[62:63], s[24:25] op_sel_hi:[1,0]
	v_pk_mul_f32 v[10:11], v[58:59], s[24:25] op_sel_hi:[1,0]
	v_pk_mul_f32 v[22:23], v[6:7], s[24:25] op_sel_hi:[1,0]
	v_pk_mul_f32 v[14:15], v[2:3], s[24:25] op_sel_hi:[1,0]
	s_add_u32 s65, s44, 0x2000000
	v_mov_b64_e32 v[28:29], v[16:17]
	v_mov_b64_e32 v[36:37], v[24:25]
	v_mov_b64_e32 v[44:45], v[16:17]
	v_mov_b64_e32 v[52:53], v[24:25]
	v_mov_b64_e32 v[68:69], v[16:17]
	v_mov_b64_e32 v[76:77], v[24:25]
	v_mov_b64_e32 v[32:33], v[12:13]
	v_mov_b64_e32 v[40:41], v[20:21]
	v_mov_b64_e32 v[48:49], v[12:13]
	v_mov_b64_e32 v[56:57], v[20:21]
	v_mov_b64_e32 v[72:73], v[12:13]
	v_mov_b64_e32 v[80:81], v[20:21]
	v_mov_b64_e32 v[84:85], v[16:17]
	v_mov_b64_e32 v[92:93], v[24:25]
	v_mov_b64_e32 v[100:101], v[16:17]
	v_mov_b64_e32 v[108:109], v[24:25]
	v_mov_b64_e32 v[116:117], v[16:17]
	v_mov_b64_e32 v[124:125], v[24:25]
	v_mov_b64_e32 v[132:133], v[16:17]
	v_mov_b64_e32 v[140:141], v[24:25]
	v_mov_b64_e32 v[88:89], v[12:13]
	v_mov_b64_e32 v[96:97], v[20:21]
	v_mov_b64_e32 v[104:105], v[12:13]
	v_mov_b64_e32 v[112:113], v[20:21]
	v_mov_b64_e32 v[120:121], v[12:13]
	v_mov_b64_e32 v[128:129], v[20:21]
	v_mov_b64_e32 v[136:137], v[12:13]
	v_mov_b64_e32 v[144:145], v[20:21]
	v_mov_b32_e32 v58, v163
	v_mov_b32_e32 v59, v153
	v_mov_b32_e32 v60, v164
	v_mov_b32_e32 v61, v153
	v_lshl_add_u32 v151, v160, 2, s46
	v_lshl_add_u32 v171, v161, 2, s46
	s_addc_u32 s66, s45, 0
	s_mov_b32 s67, -2
	s_mov_b64 s[44:45], s[16:17]
	v_mov_b64_e32 v[26:27], v[14:15]
	v_mov_b64_e32 v[34:35], v[22:23]
	v_mov_b64_e32 v[42:43], v[14:15]
	v_mov_b64_e32 v[50:51], v[22:23]
	v_mov_b64_e32 v[66:67], v[14:15]
	v_mov_b64_e32 v[74:75], v[22:23]
	v_mov_b64_e32 v[30:31], v[10:11]
	v_mov_b64_e32 v[38:39], v[18:19]
	v_mov_b64_e32 v[46:47], v[10:11]
	v_mov_b64_e32 v[54:55], v[18:19]
	v_mov_b64_e32 v[70:71], v[10:11]
	v_mov_b64_e32 v[78:79], v[18:19]
	v_mov_b64_e32 v[82:83], v[14:15]
	v_mov_b64_e32 v[90:91], v[22:23]
	v_mov_b64_e32 v[98:99], v[14:15]
	v_mov_b64_e32 v[106:107], v[22:23]
	v_mov_b64_e32 v[114:115], v[14:15]
	v_mov_b64_e32 v[122:123], v[22:23]
	v_mov_b64_e32 v[130:131], v[14:15]
	v_mov_b64_e32 v[138:139], v[22:23]
	v_mov_b64_e32 v[86:87], v[10:11]
	v_mov_b64_e32 v[94:95], v[18:19]
	v_mov_b64_e32 v[102:103], v[10:11]
	v_mov_b64_e32 v[110:111], v[18:19]
	v_mov_b64_e32 v[118:119], v[10:11]
	v_mov_b64_e32 v[126:127], v[18:19]
	v_mov_b64_e32 v[134:135], v[10:11]
	v_mov_b64_e32 v[142:143], v[18:19]
	s_branch .LBB0_1037
.LBB0_1036:
	v_add_u32_e32 v62, s58, v167
	ds_read_b128 v[2:5], v62
	ds_read_b128 v[6:9], v62 offset:1024
	ds_read_b128 v[172:175], v62 offset:2048
	ds_read_b128 v[176:179], v62 offset:3072
	v_add_u32_e32 v62, s59, v167
	ds_read_b128 v[180:183], v62
	ds_read_b128 v[184:187], v62 offset:1024
	ds_read_b128 v[188:191], v62 offset:2048
	ds_read_b128 v[192:195], v62 offset:3072
	s_add_u32 s48, s44, 0x80
	s_addc_u32 s49, s45, 0
	s_and_b64 s[46:47], s[46:47], exec
	s_cselect_b32 s49, s1, s49
	s_cselect_b32 s48, s0, s48
	s_cselect_b32 s47, s41, s66
	s_cselect_b32 s46, s40, s65
	s_mov_b32 m0, s61
	v_lshl_add_u64 v[62:63], s[44:45], 0, v[58:59]
	ds_read_b128 v[196:199], v168
	ds_read_b128 v[200:203], v168 offset:1024
	ds_read_b128 v[204:207], v168 offset:2048
	ds_read_b128 v[208:211], v168 offset:3072
	ds_read_b128 v[212:215], v168 offset:4096
	ds_read_b128 v[216:219], v168 offset:5120
	ds_read_b128 v[220:223], v168 offset:6144
	ds_read_b128 v[224:227], v168 offset:7168
	global_load_lds_dwordx4 v[62:63], off
	v_lshl_add_u64 v[62:63], s[44:45], 0, v[60:61]
	s_mov_b32 m0, s62
	s_nop 0
	global_load_lds_dwordx4 v[62:63], off
	s_waitcnt vmcnt(8)
	s_waitcnt lgkmcnt(0)
	s_barrier
; #define PG8_STAGE(bufoff, gbase, voff) do { _Pragma("unroll") for (int _i = 0; _i < 2; ++_i) \
;         __builtin_amdgcn_global_load_lds((const unsigned*)((const char*)(gbase) + (voff)[_i]), (LAS unsigned*)(lds + (bufoff) + ldsw + _i * 8192), 16, 0, 0); } while (0)
; #define PG8_LDA(dst, b, h) do { _Pragma("unroll") for (int m = 0; m < 4; ++m) { if constexpr (F8) dst##8[m] = PG8_LD32(lds + PG8_SA(b, h) + aoff + m * 2048); \
;         else { _Pragma("unroll") for (int k = 0; k < 2; ++k) dst[m][k] = *(const LAS bf16x8*)(lds + PG8_SA(b, h) + aoff + m * 2048 + k * 1024); } } } while (0)
; #define PG8_LDB(dst, b, h) do { _Pragma("unroll") for (int n = 0; n < 2; ++n) { if constexpr (F8) dst##8[n] = PG8_LD32(lds + PG8_SB(b, h) + boff + n * 2048); \
;         else { _Pragma("unroll") for (int k = 0; k < 2; ++k) dst[n][k] = *(const LAS bf16x8*)(lds + PG8_SB(b, h) + boff + n * 2048 + k * 1024); } } } while (0)
; #define PG8_WAIT_V(n) asm volatile("s_waitcnt vmcnt(" #n ")" ::: "memory")
; #define PG8_WAIT_L(n) asm volatile("s_waitcnt lgkmcnt(" #n ")" ::: "memory")
; #define PG8_BAR __builtin_amdgcn_s_barrier()
; #define PG8_SCHED __builtin_amdgcn_sched_barrier(0)
; template <class Epi, class Sched, bool GATHER, bool F8 = false>
; __device__ __forceinline__ void gemm_phase(LAS unsigned char* lds, const int K, const Sched& S, const Epi& E) {
;     ...
;             PG8_LDB(B0, 0, 0); PG8_LDB(B1, 0, 1); PG8_SCHED; PG8_LDA(At, 0, 0); PG8_STAGE(PG8_SA(1, 1), a1, vA[1]);
;             PG8_WAIT_V(8); PG8_WAIT_L(0); PG8_BAR; PG8_MMA(0, 0, At, B0); PG8_MMA(0, 1, At, B1); PG8_BAR; PG8_SCHED;
;             PG8_LDA(At, 0, 1); PG8_STAGE(PG8_SB(0, 0), b2, voffB); PG8_STAGE(PG8_SB(0, 1), b2 + hstepB, voffB); PG8_STAGE(PG8_SA(0, 0), a2, vN[0]);
;             PG8_WAIT_V(8); PG8_WAIT_L(0); PG8_BAR; PG8_MMA(1, 0, At, B0); PG8_MMA(1, 1, At, B1); PG8_BAR; PG8_SCHED;
;             PG8_LDB(B0, 1, 0); PG8_LDB(B1, 1, 1); PG8_SCHED; PG8_LDA(At, 1, 0); PG8_STAGE(PG8_SA(0, 1), a2, vN[1]);
;             PG8_WAIT_V(8); PG8_WAIT_L(0); PG8_BAR; PG8_MMA(0, 0, At, B0); PG8_MMA(0, 1, At, B1); PG8_BAR; PG8_SCHED;
	s_setprio 1
	s_waitcnt lgkmcnt(0)
	v_mfma_scale_f32_16x16x128_f8f6f4 v[142:145], v[2:9], v[196:203], v[142:145], v165, v165 op_sel_hi:[0,0,0]
	v_mfma_scale_f32_16x16x128_f8f6f4 v[134:137], v[172:179], v[196:203], v[134:137], v165, v165 op_sel_hi:[0,0,0]
	v_mfma_scale_f32_16x16x128_f8f6f4 v[126:129], v[2:9], v[204:211], v[126:129], v165, v165 op_sel_hi:[0,0,0]
	v_mfma_scale_f32_16x16x128_f8f6f4 v[118:121], v[172:179], v[204:211], v[118:121], v165, v165 op_sel_hi:[0,0,0]
	v_mfma_scale_f32_16x16x128_f8f6f4 v[110:113], v[2:9], v[212:219], v[110:113], v165, v165 op_sel_hi:[0,0,0]
	v_mfma_scale_f32_16x16x128_f8f6f4 v[102:105], v[172:179], v[212:219], v[102:105], v165, v165 op_sel_hi:[0,0,0]
	v_mfma_scale_f32_16x16x128_f8f6f4 v[94:97], v[2:9], v[220:227], v[94:97], v165, v165 op_sel_hi:[0,0,0]
	v_mfma_scale_f32_16x16x128_f8f6f4 v[86:89], v[172:179], v[220:227], v[86:89], v165, v165 op_sel_hi:[0,0,0]
	s_setprio 0
	s_setprio 1
	v_mfma_scale_f32_16x16x128_f8f6f4 v[138:141], v[180:187], v[196:203], v[138:141], v165, v165 op_sel_hi:[0,0,0]
	v_mfma_scale_f32_16x16x128_f8f6f4 v[130:133], v[188:195], v[196:203], v[130:133], v165, v165 op_sel_hi:[0,0,0]
	v_mfma_scale_f32_16x16x128_f8f6f4 v[122:125], v[180:187], v[204:211], v[122:125], v165, v165 op_sel_hi:[0,0,0]
	v_mfma_scale_f32_16x16x128_f8f6f4 v[114:117], v[188:195], v[204:211], v[114:117], v165, v165 op_sel_hi:[0,0,0]
	v_mfma_scale_f32_16x16x128_f8f6f4 v[106:109], v[180:187], v[212:219], v[106:109], v165, v165 op_sel_hi:[0,0,0]
	v_mfma_scale_f32_16x16x128_f8f6f4 v[98:101], v[188:195], v[212:219], v[98:101], v165, v165 op_sel_hi:[0,0,0]
	v_mfma_scale_f32_16x16x128_f8f6f4 v[90:93], v[180:187], v[220:227], v[90:93], v165, v165 op_sel_hi:[0,0,0]
	v_mfma_scale_f32_16x16x128_f8f6f4 v[82:85], v[188:195], v[220:227], v[82:85], v165, v165 op_sel_hi:[0,0,0]
	s_setprio 0
	s_barrier
	s_add_i32 s68, s58, s37
	v_lshl_add_u64 v[62:63], s[46:47], 0, v[148:149]
	s_mov_b32 m0, s68
	ds_read_b128 v[196:199], v168 offset:16384
	ds_read_b128 v[200:203], v168 offset:17408
	ds_read_b128 v[204:207], v168 offset:18432
	ds_read_b128 v[208:211], v168 offset:19456
	ds_read_b128 v[212:215], v168 offset:20480
	ds_read_b128 v[216:219], v168 offset:21504
	ds_read_b128 v[220:223], v168 offset:22528
	ds_read_b128 v[224:227], v168 offset:23552
	global_load_lds_dwordx4 v[62:63], off
	s_add_i32 m0, s68, 0x2000
	s_add_u32 s68, s46, 0x4000
	v_lshl_add_u64 v[64:65], s[46:47], 0, v[146:147]
	s_addc_u32 s69, s47, 0
	s_add_i32 s70, s59, s37
	global_load_lds_dwordx4 v[64:65], off
	v_lshl_add_u64 v[156:157], s[68:69], 0, v[148:149]
	s_mov_b32 m0, s70
	v_mov_b32_e32 v155, v153
	global_load_lds_dwordx4 v[156:157], off
	v_lshl_add_u64 v[156:157], s[68:69], 0, v[146:147]
	s_add_i32 m0, s70, 0x2000
	v_lshl_add_u64 v[158:159], s[48:49], 0, v[152:153]
	global_load_lds_dwordx4 v[156:157], off
	s_mov_b32 m0, s51
	v_lshl_add_u64 v[156:157], s[48:49], 0, v[154:155]
	global_load_lds_dwordx4 v152, s[48:49]
	s_mov_b32 m0, s52
	s_nop 0
	global_load_lds_dwordx4 v154, s[48:49]
	s_waitcnt vmcnt(8)
	s_waitcnt lgkmcnt(0)
	s_barrier
	s_setprio 1
	s_waitcnt lgkmcnt(0)
	v_mfma_scale_f32_16x16x128_f8f6f4 v[78:81], v[2:9], v[196:203], v[78:81], v165, v165 op_sel_hi:[0,0,0]
	v_mfma_scale_f32_16x16x128_f8f6f4 v[70:73], v[172:179], v[196:203], v[70:73], v165, v165 op_sel_hi:[0,0,0]
	v_mfma_scale_f32_16x16x128_f8f6f4 v[54:57], v[2:9], v[204:211], v[54:57], v165, v165 op_sel_hi:[0,0,0]
	v_mfma_scale_f32_16x16x128_f8f6f4 v[46:49], v[172:179], v[204:211], v[46:49], v165, v165 op_sel_hi:[0,0,0]
	v_mfma_scale_f32_16x16x128_f8f6f4 v[38:41], v[2:9], v[212:219], v[38:41], v165, v165 op_sel_hi:[0,0,0]
	v_mfma_scale_f32_16x16x128_f8f6f4 v[30:33], v[172:179], v[212:219], v[30:33], v165, v165 op_sel_hi:[0,0,0]
	v_mfma_scale_f32_16x16x128_f8f6f4 v[18:21], v[2:9], v[220:227], v[18:21], v165, v165 op_sel_hi:[0,0,0]
	v_mfma_scale_f32_16x16x128_f8f6f4 v[10:13], v[172:179], v[220:227], v[10:13], v165, v165 op_sel_hi:[0,0,0]
	s_setprio 0
	s_setprio 1
	v_mfma_scale_f32_16x16x128_f8f6f4 v[74:77], v[180:187], v[196:203], v[74:77], v165, v165 op_sel_hi:[0,0,0]
	v_mfma_scale_f32_16x16x128_f8f6f4 v[66:69], v[188:195], v[196:203], v[66:69], v165, v165 op_sel_hi:[0,0,0]
	v_mfma_scale_f32_16x16x128_f8f6f4 v[50:53], v[180:187], v[204:211], v[50:53], v165, v165 op_sel_hi:[0,0,0]
	v_mfma_scale_f32_16x16x128_f8f6f4 v[42:45], v[188:195], v[204:211], v[42:45], v165, v165 op_sel_hi:[0,0,0]
	v_mfma_scale_f32_16x16x128_f8f6f4 v[34:37], v[180:187], v[212:219], v[34:37], v165, v165 op_sel_hi:[0,0,0]
	v_mfma_scale_f32_16x16x128_f8f6f4 v[26:29], v[188:195], v[212:219], v[26:29], v165, v165 op_sel_hi:[0,0,0]
	v_mfma_scale_f32_16x16x128_f8f6f4 v[22:25], v[180:187], v[220:227], v[22:25], v165, v165 op_sel_hi:[0,0,0]
	v_mfma_scale_f32_16x16x128_f8f6f4 v[14:17], v[188:195], v[220:227], v[14:17], v165, v165 op_sel_hi:[0,0,0]
	s_setprio 0
	s_barrier
	s_add_i32 s68, 0, 0x18000
	s_add_i32 s69, 0, 0x1c000
	v_add_u32_e32 v2, s68, v167
	v_add_u32_e32 v155, s69, v167
	ds_read_b128 v[172:175], v2
	ds_read_b128 v[176:179], v2 offset:1024
	ds_read_b128 v[180:183], v2 offset:2048
	ds_read_b128 v[184:187], v2 offset:3072
	ds_read_b128 v[2:5], v155
	ds_read_b128 v[6:9], v155 offset:1024
	ds_read_b128 v[188:191], v155 offset:2048
	ds_read_b128 v[192:195], v155 offset:3072
	s_mov_b32 m0, s53
	ds_read_b128 v[196:199], v168 offset:32768
	ds_read_b128 v[200:203], v168 offset:33792
	ds_read_b128 v[204:207], v168 offset:34816
	ds_read_b128 v[208:211], v168 offset:35840
	ds_read_b128 v[212:215], v168 offset:36864
	ds_read_b128 v[216:219], v168 offset:37888
	ds_read_b128 v[220:223], v168 offset:38912
	ds_read_b128 v[224:227], v168 offset:39936
	global_load_lds_dwordx4 v163, s[48:49]
	s_mov_b32 m0, s54
	s_nop 0
	global_load_lds_dwordx4 v164, s[48:49]
	s_waitcnt vmcnt(8)
	s_waitcnt lgkmcnt(0)
	s_barrier
; #define PG8_STAGE(bufoff, gbase, voff) do { _Pragma("unroll") for (int _i = 0; _i < 2; ++_i) \
;         __builtin_amdgcn_global_load_lds((const unsigned*)((const char*)(gbase) + (voff)[_i]), (LAS unsigned*)(lds + (bufoff) + ldsw + _i * 8192), 16, 0, 0); } while (0)
; #define PG8_LDA(dst, b, h) do { _Pragma("unroll") for (int m = 0; m < 4; ++m) { if constexpr (F8) dst##8[m] = PG8_LD32(lds + PG8_SA(b, h) + aoff + m * 2048); \
;         else { _Pragma("unroll") for (int k = 0; k < 2; ++k) dst[m][k] = *(const LAS bf16x8*)(lds + PG8_SA(b, h) + aoff + m * 2048 + k * 1024); } } } while (0)
; #define PG8_LDB(dst, b, h) do { _Pragma("unroll") for (int n = 0; n < 2; ++n) { if constexpr (F8) dst##8[n] = PG8_LD32(lds + PG8_SB(b, h) + boff + n * 2048); \
;         else { _Pragma("unroll") for (int k = 0; k < 2; ++k) dst[n][k] = *(const LAS bf16x8*)(lds + PG8_SB(b, h) + boff + n * 2048 + k * 1024); } } } while (0)
; #define PG8_WAIT_V(n) asm volatile("s_waitcnt vmcnt(" #n ")" ::: "memory")
; #define PG8_WAIT_L(n) asm volatile("s_waitcnt lgkmcnt(" #n ")" ::: "memory")
; #define PG8_BAR __builtin_amdgcn_s_barrier()
; #define PG8_SCHED __builtin_amdgcn_sched_barrier(0)
; template <class Epi, class Sched, bool GATHER, bool F8 = false>
; __device__ __forceinline__ void gemm_phase(LAS unsigned char* lds, const int K, const Sched& S, const Epi& E) {
;     ...
;             PG8_LDB(B0, 1, 0); PG8_LDB(B1, 1, 1); PG8_SCHED; PG8_LDA(At, 1, 0); PG8_STAGE(PG8_SA(0, 1), a2, vN[1]);
;             PG8_WAIT_V(8); PG8_WAIT_L(0); PG8_BAR; PG8_MMA(0, 0, At, B0); PG8_MMA(0, 1, At, B1); PG8_BAR; PG8_SCHED;
;             PG8_LDA(At, 1, 1); PG8_STAGE(PG8_SB(1, 0), b3, voffB); PG8_STAGE(PG8_SB(1, 1), b3 + hstepB, voffB); PG8_STAGE(PG8_SA(1, 0), a3, vN[0]);
;             PG8_WAIT_V(8); PG8_WAIT_L(0); PG8_BAR; PG8_MMA(1, 0, At, B0); PG8_MMA(1, 1, At, B1); PG8_BAR; PG8_SCHED;
;         }
	s_setprio 1
	s_waitcnt lgkmcnt(0)
	v_mfma_scale_f32_16x16x128_f8f6f4 v[142:145], v[172:179], v[196:203], v[142:145], v165, v165 op_sel_hi:[0,0,0]
	v_mfma_scale_f32_16x16x128_f8f6f4 v[134:137], v[180:187], v[196:203], v[134:137], v165, v165 op_sel_hi:[0,0,0]
	v_mfma_scale_f32_16x16x128_f8f6f4 v[126:129], v[172:179], v[204:211], v[126:129], v165, v165 op_sel_hi:[0,0,0]
	v_mfma_scale_f32_16x16x128_f8f6f4 v[118:121], v[180:187], v[204:211], v[118:121], v165, v165 op_sel_hi:[0,0,0]
	v_mfma_scale_f32_16x16x128_f8f6f4 v[110:113], v[172:179], v[212:219], v[110:113], v165, v165 op_sel_hi:[0,0,0]
	v_mfma_scale_f32_16x16x128_f8f6f4 v[102:105], v[180:187], v[212:219], v[102:105], v165, v165 op_sel_hi:[0,0,0]
	v_mfma_scale_f32_16x16x128_f8f6f4 v[94:97], v[172:179], v[220:227], v[94:97], v165, v165 op_sel_hi:[0,0,0]
	v_mfma_scale_f32_16x16x128_f8f6f4 v[86:89], v[180:187], v[220:227], v[86:89], v165, v165 op_sel_hi:[0,0,0]
	s_setprio 0
	s_setprio 1
	v_mfma_scale_f32_16x16x128_f8f6f4 v[138:141], v[2:9], v[196:203], v[138:141], v165, v165 op_sel_hi:[0,0,0]
	v_mfma_scale_f32_16x16x128_f8f6f4 v[130:133], v[188:195], v[196:203], v[130:133], v165, v165 op_sel_hi:[0,0,0]
	v_mfma_scale_f32_16x16x128_f8f6f4 v[122:125], v[2:9], v[204:211], v[122:125], v165, v165 op_sel_hi:[0,0,0]
	v_mfma_scale_f32_16x16x128_f8f6f4 v[114:117], v[188:195], v[204:211], v[114:117], v165, v165 op_sel_hi:[0,0,0]
	v_mfma_scale_f32_16x16x128_f8f6f4 v[106:109], v[2:9], v[212:219], v[106:109], v165, v165 op_sel_hi:[0,0,0]
	v_mfma_scale_f32_16x16x128_f8f6f4 v[98:101], v[188:195], v[212:219], v[98:101], v165, v165 op_sel_hi:[0,0,0]
	v_mfma_scale_f32_16x16x128_f8f6f4 v[90:93], v[2:9], v[220:227], v[90:93], v165, v165 op_sel_hi:[0,0,0]
	v_mfma_scale_f32_16x16x128_f8f6f4 v[82:85], v[188:195], v[220:227], v[82:85], v165, v165 op_sel_hi:[0,0,0]
	s_setprio 0
	s_barrier
	s_add_i32 s48, s68, s37
	v_lshl_add_u64 v[62:63], v[62:63], 0, s[100:101]
	s_mov_b32 m0, s48
	ds_read_b128 v[196:199], v168 offset:49152
	ds_read_b128 v[200:203], v168 offset:50176
	ds_read_b128 v[204:207], v168 offset:51200
	ds_read_b128 v[208:211], v168 offset:52224
	ds_read_b128 v[212:215], v168 offset:53248
	ds_read_b128 v[216:219], v168 offset:54272
	ds_read_b128 v[220:223], v168 offset:55296
	ds_read_b128 v[224:227], v168 offset:56320
	global_load_lds_dwordx4 v[62:63], off
	s_add_i32 m0, s48, 0x2000
	s_add_u32 s46, s46, 0x1004000
	v_lshl_add_u64 v[62:63], v[64:65], 0, s[100:101]
	s_addc_u32 s47, s47, 0
	s_add_i32 s48, s69, s37
	global_load_lds_dwordx4 v[62:63], off
	v_lshl_add_u64 v[62:63], s[46:47], 0, v[148:149]
	s_mov_b32 m0, s48
	s_nop 0
	global_load_lds_dwordx4 v[62:63], off
	v_lshl_add_u64 v[62:63], s[46:47], 0, v[146:147]
	s_add_i32 m0, s48, 0x2000
	s_nop 0
	global_load_lds_dwordx4 v[62:63], off
	v_lshl_add_u64 v[62:63], v[158:159], 0, s[14:15]
	s_mov_b32 m0, s55
	s_nop 0
	global_load_lds_dwordx4 v[62:63], off
	v_lshl_add_u64 v[62:63], v[156:157], 0, s[14:15]
	s_mov_b32 m0, s56
	s_nop 0
	global_load_lds_dwordx4 v[62:63], off
	s_waitcnt vmcnt(8)
	s_waitcnt lgkmcnt(0)
	s_barrier
	s_setprio 1
	s_waitcnt lgkmcnt(0)
	v_mfma_scale_f32_16x16x128_f8f6f4 v[78:81], v[172:179], v[196:203], v[78:81], v165, v165 op_sel_hi:[0,0,0]
	v_mfma_scale_f32_16x16x128_f8f6f4 v[70:73], v[180:187], v[196:203], v[70:73], v165, v165 op_sel_hi:[0,0,0]
	v_mfma_scale_f32_16x16x128_f8f6f4 v[54:57], v[172:179], v[204:211], v[54:57], v165, v165 op_sel_hi:[0,0,0]
	v_mfma_scale_f32_16x16x128_f8f6f4 v[46:49], v[180:187], v[204:211], v[46:49], v165, v165 op_sel_hi:[0,0,0]
	v_mfma_scale_f32_16x16x128_f8f6f4 v[38:41], v[172:179], v[212:219], v[38:41], v165, v165 op_sel_hi:[0,0,0]
	v_mfma_scale_f32_16x16x128_f8f6f4 v[30:33], v[180:187], v[212:219], v[30:33], v165, v165 op_sel_hi:[0,0,0]
	v_mfma_scale_f32_16x16x128_f8f6f4 v[18:21], v[172:179], v[220:227], v[18:21], v165, v165 op_sel_hi:[0,0,0]
	v_mfma_scale_f32_16x16x128_f8f6f4 v[10:13], v[180:187], v[220:227], v[10:13], v165, v165 op_sel_hi:[0,0,0]
	s_setprio 0
	s_setprio 1
	v_mfma_scale_f32_16x16x128_f8f6f4 v[74:77], v[2:9], v[196:203], v[74:77], v165, v165 op_sel_hi:[0,0,0]
	v_mfma_scale_f32_16x16x128_f8f6f4 v[66:69], v[188:195], v[196:203], v[66:69], v165, v165 op_sel_hi:[0,0,0]
	v_mfma_scale_f32_16x16x128_f8f6f4 v[50:53], v[2:9], v[204:211], v[50:53], v165, v165 op_sel_hi:[0,0,0]
	v_mfma_scale_f32_16x16x128_f8f6f4 v[42:45], v[188:195], v[204:211], v[42:45], v165, v165 op_sel_hi:[0,0,0]
	v_mfma_scale_f32_16x16x128_f8f6f4 v[34:37], v[2:9], v[212:219], v[34:37], v165, v165 op_sel_hi:[0,0,0]
	v_mfma_scale_f32_16x16x128_f8f6f4 v[26:29], v[188:195], v[212:219], v[26:29], v165, v165 op_sel_hi:[0,0,0]
	v_mfma_scale_f32_16x16x128_f8f6f4 v[22:25], v[2:9], v[220:227], v[22:25], v165, v165 op_sel_hi:[0,0,0]
	v_mfma_scale_f32_16x16x128_f8f6f4 v[14:17], v[188:195], v[220:227], v[14:17], v165, v165 op_sel_hi:[0,0,0]
	s_setprio 0
	s_barrier
	s_add_i32 s67, s67, 2
	s_add_u32 s44, s44, 0x100
	s_addc_u32 s45, s45, 0
	s_add_u32 s65, s65, 0x2000000
	s_addc_u32 s66, s66, 0
	s_cmp_gt_u32 s67, 13
	s_cbranch_scc1 .LBB0_1039

; #define PG8_WAIT_V(n) asm volatile("s_waitcnt vmcnt(" #n ")" ::: "memory")
; #define PG8_BAR __builtin_amdgcn_s_barrier()
; template <class Epi, class Sched, bool GATHER, bool F8 = false>
; __device__ __forceinline__ void gemm_phase(LAS unsigned char* lds, const int K, const Sched& S, const Epi& E) {
;     ...
;     Unit cur, nxt; int ui = 0;
;     if (!S.next(0, cur)) return;
;     if constexpr (GATHER) { S.offsets(0, RA, CA, vA); }
; #pragma unroll
;     for (int h = 0; h < 2; ++h)
; #pragma unroll
;         for (int i = 0; i < 2; ++i) vN[h][i] = vA[h][i];
;     f32x4 acc[2][2][4][2];
; #pragma unroll
;     for (int a = 0; a < 2; ++a)
; #pragma unroll
;         for (int b = 0; b < 2; ++b)
; #pragma unroll
;             for (int m = 0; m < 4; ++m)
; #pragma unroll
;                 for (int n = 0; n < 2; ++n) acc[a][b][m][n] = (f32x4){0.f, 0.f, 0.f, 0.f};
;     if constexpr (EpiInit<Epi>::value) { const typename EpiInit<Epi>::Pre p0 = E.preload(cur, wr, wc, fr, fq); E.init(acc, p0); }
;     int one_scale = 0x7f7f7f7f; asm volatile("" : "+v"(one_scale));
;     bf16x8 At[4][2], B0[2][2], B1[2][2]; i32x8 At8[4], B08[2], B18[2];
;     const char* cA = cur.A; const char* cB = cur.B;
;     PG8_STAGE(PG8_SB(0, 0), cB, voffB); PG8_STAGE(PG8_SB(0, 1), cB + hstepB, voffB); PG8_STAGE(PG8_SA(0, 0), cA, vA[0]); PG8_STAGE(PG8_SA(0, 1), cA, vA[1]);
;     if (wr == 1) PG8_BAR;
;     PG8_WAIT_V(2); PG8_BAR;
;     PG8_STAGE(PG8_SB(1, 0), cB + kstep, voffB); PG8_STAGE(PG8_SA(1, 0), cA + kstep, vA[0]); PG8_STAGE(PG8_SB(1, 1), cB + hstepB + kstep, voffB);
;     PG8_WAIT_V(6); PG8_BAR;
;     __device__ __forceinline__ bool next(int i, Unit& u) const {
;         const int x = c & 7, j = c >> 3, tile = 32 * i + 4 * x + (j & 3), pn = j >> 2;
;         if (tile >= tb.ntiles) return false;
;         const int e = tb.tile_e[tile];
;         u.A = H + (size_t)tile * 256 * DFF; u.B = W + ((size_t)e * DM + pn * 256) * DFF; u.row0 = tile * 256; u.col0 = pn * 256; u.tag = e; u.aux = 0; return true;
;     }
;     __device__ __forceinline__ Pre preload(const Unit& u, int wr, int wc, int fr, int fq) const {
;         const float* pb = bd + (size_t)u.tag * DM + u.col0 + wc * 64 + 8 * fq;
;         Pre p;
; #pragma unroll
;         for (int bj = 0; bj < 2; ++bj)
; #pragma unroll
;             for (int n = 0; n < 2; ++n) p.bv[bj][n] = *(const f32x4*)(pb + bj * 32 + 4 * n);
;         return p;
;     }
.LBB0_1119:
	s_add_i32 s0, 0, 0x20600
	v_mov_b32_e32 v1, s0
	ds_read_b32 v1, v1
	s_lshl_b32 s0, s2, 2
	s_and_b32 s0, s0, 28
	s_bfe_u32 s1, s2, 0x20003
	s_or_b32 s6, s0, s1
	s_waitcnt lgkmcnt(0)
	v_cmp_ge_i32_e32 vcc, s6, v1
	v_readfirstlane_b32 s20, v0
	s_cbranch_vccnz .LBB0_1135
	s_add_u32 s7, s82, 0x34000000
	s_addc_u32 s23, s83, 0
	s_add_u32 s18, s82, 0x24000000
	s_waitcnt vmcnt(0)
	v_lshlrev_b32_e32 v2, 4, v0
	s_addc_u32 s22, s83, 0
	s_lshr_b32 s0, s20, 6
	v_or_b32_e32 v18, 0x2000, v2
	v_and_b32_e32 v5, 32, v0
	s_lshl_b32 s25, s0, 10
	v_lshrrev_b32_e32 v3, 7, v18
	v_bfe_u32 v21, v0, 2, 4
	s_movk_i32 s0, 0x70
	v_bitop3_b32 v19, v2, v5, 48 bitop3:0x6c
	v_and_b32_e32 v20, 64, v0
	v_and_or_b32 v3, v3, s0, v21
	v_or_b32_e32 v2, v19, v20
	v_lshl_or_b32 v146, v3, 11, v2
	v_lshrrev_b32_e32 v3, 5, v0
	v_lshrrev_b32_e32 v6, 1, v0
	v_and_b32_e32 v3, 4, v3
	v_bfe_u32 v5, v0, 2, 2
	v_and_b32_e32 v6, 24, v6
	v_or3_b32 v3, v3, v5, v6
	v_lshrrev_b32_e32 v5, 6, v18
	s_movk_i32 s0, 0xc0
	v_and_or_b32 v5, v5, s0, v3
	s_lshl_b32 s0, s6, 2
	s_add_i32 s0, s0, 0
	s_add_i32 s0, s0, 0x20000
	v_mov_b32_e32 v6, s0
	ds_read_b32 v6, v6
	s_bfe_u32 s16, s20, 0x20006
	s_lshr_b32 s17, s20, 8
	s_lshl_b32 s0, s6, 19
	v_lshrrev_b32_e32 v4, 2, v0
	s_waitcnt lgkmcnt(0)
	v_readfirstlane_b32 s12, v6
	s_ashr_i32 s13, s12, 31
	s_add_u32 s44, s7, s0
	s_addc_u32 s45, s23, 0
	s_lshl_b32 s0, s2, 3
	s_and_b32 s0, s0, 0xffffff00
	s_ashr_i32 s1, s0, 31
	s_lshl_b64 s[2:3], s[12:13], 18
	s_lshl_b64 s[4:5], s[0:1], 7
	s_add_u32 s2, s18, s2
	s_addc_u32 s3, s22, s3
	s_add_u32 s46, s2, s4
	s_addc_u32 s47, s3, s5
	s_lshl_b64 s[2:3], s[12:13], 13
	s_add_u32 s13, s26, s2
	s_addc_u32 s14, s27, s3
	s_lshl_b64 s[2:3], s[0:1], 2
	s_add_u32 s1, s13, s2
	s_addc_u32 s3, s14, s3
	s_lshl_b32 s50, s16, 6
	s_lshl_b32 s2, s16, 8
	s_add_u32 s2, s1, s2
	v_bfe_u32 v22, v0, 4, 2
	v_lshl_or_b32 v150, v5, 11, v2
	v_lshrrev_b32_e32 v254, 11, v150
	v_and_b32_e32 v150, 0x7f, v150
	v_lshl_or_b32 v150, v254, 7, v150
	v_lshrrev_b32_e32 v5, 3, v0
	v_and_or_b32 v3, v4, 64, v3
	s_addc_u32 s3, s3, 0
	s_add_i32 s51, s25, 0
	v_and_or_b32 v5, v5, 48, v21
	v_lshl_or_b32 v156, v3, 11, v2
	v_lshrrev_b32_e32 v254, 11, v156
	v_and_b32_e32 v156, 0x7f, v156
	v_lshl_or_b32 v156, v254, 7, v156
	v_lshlrev_b32_e32 v10, 5, v22
	v_mov_b32_e32 v162, 0x7f7f7f7f
	s_add_i32 m0, s51, 0x10000
	v_lshl_or_b32 v152, v5, 11, v2
	global_load_dwordx4 v[74:77], v10, s[2:3] offset:16
	global_load_dwordx4 v[78:81], v10, s[2:3]
	global_load_dwordx4 v[2:5], v10, s[2:3] offset:144
	global_load_dwordx4 v[6:9], v10, s[2:3] offset:128
	global_load_lds_dwordx4 v156, s[46:47]
	s_add_i32 m0, s51, 0x12000
	s_add_u32 s2, s46, 0x1000
	global_load_lds_dwordx4 v150, s[46:47]
	s_addc_u32 s3, s47, 0
	s_add_i32 m0, s51, 0x14000
	s_add_i32 s52, s51, 0x2000
	global_load_lds_dwordx4 v156, s[2:3]
	s_add_i32 m0, s51, 0x16000
	s_add_i32 s53, s51, 0x4000
	global_load_lds_dwordx4 v150, s[2:3]
	s_mov_b32 m0, s51
	v_or_b32_e32 v154, 0x40000, v152
	global_load_lds_dwordx4 v152, s[44:45]
	s_mov_b32 m0, s52
	s_add_i32 s54, s51, 0x6000
	global_load_lds_dwordx4 v146, s[44:45]
	s_mov_b32 m0, s53
	v_or_b32_e32 v148, 0x40000, v146
	global_load_lds_dwordx4 v154, s[44:45]
	s_mov_b32 m0, s54
	v_mov_b32_e32 v157, 0
	global_load_lds_dwordx4 v148, s[44:45]
	v_mov_b32_e32 v151, v157
	v_mov_b32_e32 v153, v157
	v_mov_b32_e32 v147, v157
	s_cmp_eq_u32 s17, 1
	v_lshlrev_b32_e32 v23, 3, v22
	v_lshl_add_u64 v[16:17], s[46:47], 0, v[156:157]
	v_lshl_add_u64 v[14:15], s[46:47], 0, v[150:151]
	v_lshl_add_u64 v[10:11], s[44:45], 0, v[152:153]
	s_cselect_b64 s[2:3], -1, 0
	s_cmp_lg_u32 s17, 1
	v_lshl_add_u64 v[12:13], s[44:45], 0, v[146:147]
	s_cbranch_scc1 .LBB0_1122
	s_barrier
.LBB0_1122:
	s_lshl_b32 s64, s6, 8
	s_add_u32 s14, s82, 0x44600000
	s_addc_u32 s15, s83, 0
	s_lshl_b32 s55, s17, 6
	s_lshl_b32 s1, s17, 13
	s_lshl_b32 s13, s16, 12
	s_mov_b64 s[16:17], 0x80
	s_mov_b64 s[100:101], 0x800000
	s_add_i32 m0, s51, 0x18000
	v_lshl_add_u64 v[16:17], v[16:17], 0, s[100:101]
	s_waitcnt vmcnt(2)
	s_barrier
	global_load_lds_dwordx4 v[16:17], off
	v_lshl_add_u64 v[14:15], v[14:15], 0, s[100:101]
	s_add_i32 m0, s51, 0x1a000
	s_add_i32 s56, s51, 0x8000
	s_add_i32 s57, s51, 0xa000
	global_load_lds_dwordx4 v[14:15], off
	v_lshl_add_u64 v[10:11], v[10:11], 0, s[16:17]
	s_mov_b32 m0, s56
	s_add_u32 s36, s46, 0x801000
	global_load_lds_dwordx4 v[10:11], off
	v_lshl_add_u64 v[10:11], v[12:13], 0, s[16:17]
	s_mov_b32 m0, s57
	s_addc_u32 s37, s47, 0
	global_load_lds_dwordx4 v[10:11], off
	s_add_i32 m0, s51, 0x1c000
	v_lshl_add_u64 v[10:11], s[36:37], 0, v[156:157]
	global_load_lds_dwordx4 v[10:11], off
	v_lshl_add_u64 v[10:11], s[36:37], 0, v[150:151]
	s_add_i32 m0, s51, 0x1e000
	v_lshlrev_b32_e32 v13, 2, v0
	global_load_lds_dwordx4 v[10:11], off
	v_and_b32_e32 v10, 15, v0
	v_lshlrev_b32_e32 v11, 4, v22
	v_lshl_or_b32 v12, v10, 6, v11
	v_and_b32_e32 v13, 32, v13
	s_cmpk_lt_u32 s20, 0x100
	v_bitop3_b32 v12, v12, s1, v13 bitop3:0xde
	v_lshlrev_b32_e32 v14, 6, v0
	s_movk_i32 s1, 0x3c0
	s_cselect_b64 s[20:21], -1, 0
	s_add_u32 s58, s18, s4
	v_and_or_b32 v14, v14, s1, v11
	s_addc_u32 s59, s22, s5
	s_add_i32 s4, 0, 0x20800
	v_bitop3_b32 v163, s13, v14, v13 bitop3:0xf6
	v_lshrrev_b32_e32 v13, 6, v0
	s_movk_i32 s5, 0x900
	v_mov_b32_e32 v16, s4
	v_and_b32_e32 v14, 7, v0
	s_movk_i32 s1, 0x90
	v_mad_u32_u24 v13, v13, s5, v16
	v_lshl_or_b32 v164, v14, 3, s50
	v_mad_u32_u24 v10, v10, s1, v13
	v_lshl_add_u32 v13, v14, 4, v13
	v_lshlrev_b32_e32 v14, 8, v0
	v_and_b32_e32 v14, 0x18000, v14
	v_lshlrev_b32_e32 v16, 11, v21
	v_or3_b32 v14, v19, v14, v16
	v_add_u32_e32 v14, v14, v20
	v_or_b32_e32 v158, 0x40000, v14
	v_lshlrev_b32_e32 v14, 4, v18
	v_and_b32_e32 v14, 0x38000, v14
	s_waitcnt vmcnt(6)
	v_bfe_u32 v165, v0, 3, 3
	v_or3_b32 v14, v19, v14, v16
	v_mul_u32_u24_e32 v15, 0x90, v165
	v_add_u32_e32 v14, v14, v20
	v_mov_b32_e32 v155, v157
	v_mov_b32_e32 v149, v157
	s_mov_b32 s19, 0
	v_or_b32_e32 v166, 8, v165
	v_mov_b32_e32 v159, v157
	v_or_b32_e32 v160, 0x40000, v14
	v_mov_b32_e32 v161, v157
	s_mov_b32 s22, 0x42800000
	s_add_i32 s60, 0, 0x10000
	s_add_i32 s61, 0, 0x14000
	v_add_u32_e32 v167, 0, v12
	v_lshlrev_b32_e32 v168, 2, v23
	s_mov_b32 s24, 0x3c800000
	v_add_u32_e32 v169, v10, v11
	v_add_u32_e32 v171, v13, v15
	s_mov_b32 s62, 0
	s_barrier
	s_branch .LBB0_1125

; template <class Epi, class Sched, bool GATHER, bool F8 = false>
; __device__ __forceinline__ void gemm_phase(LAS unsigned char* lds, const int K, const Sched& S, const Epi& E) {
;     ...
;     for (;;) {
;         const bool has_next = S.next(ui + 1, nxt);
;         const char* nA = has_next ? nxt.A : cA; const char* nB = has_next ? nxt.B : cB;
;         for (int t = 0; t < nt; t += 2) {
;             const bool last = (t == nt - 2);
;             const char* a1 = cA + (size_t)(t + 1) * kstep;
;             const char* a2 = last ? nA : cA + (size_t)(t + 2) * kstep; const char* b2 = last ? nB : cB + (size_t)(t + 2) * kstep;
;             const char* a3 = a2 + kstep; const char* b3 = b2 + kstep;
;             if constexpr (GATHER) { if (last && has_next) S.offsets(ui + 1, RA, CA, vN); }
;             PG8_LDB(B0, 0, 0); PG8_LDB(B1, 0, 1); PG8_SCHED; PG8_LDA(At, 0, 0); PG8_STAGE(PG8_SA(1, 1), a1, vA[1]);
;             PG8_WAIT_V(8); PG8_WAIT_L(0); PG8_BAR; PG8_MMA(0, 0, At, B0); PG8_MMA(0, 1, At, B1); PG8_BAR; PG8_SCHED;
;             PG8_LDA(At, 0, 1); PG8_STAGE(PG8_SB(0, 0), b2, voffB); PG8_STAGE(PG8_SB(0, 1), b2 + hstepB, voffB); PG8_STAGE(PG8_SA(0, 0), a2, vN[0]);
;             PG8_WAIT_V(8); PG8_WAIT_L(0); PG8_BAR; PG8_MMA(1, 0, At, B0); PG8_MMA(1, 1, At, B1); PG8_BAR; PG8_SCHED;
;     __device__ __forceinline__ bool next(int i, Unit& u) const {
;         const int x = c & 7, j = c >> 3, tile = 32 * i + 4 * x + (j & 3), pn = j >> 2;
;         if (tile >= tb.ntiles) return false;
;         const int e = tb.tile_e[tile];
;         u.A = H + (size_t)tile * 256 * DFF; u.B = W + ((size_t)e * DM + pn * 256) * DFF; u.row0 = tile * 256; u.col0 = pn * 256; u.tag = e; u.aux = 0; return true;
;     }
;     __device__ __forceinline__ Pre preload(const Unit& u, int wr, int wc, int fr, int fq) const {
;         const float* pb = bd + (size_t)u.tag * DM + u.col0 + wc * 64 + 8 * fq;
;         Pre p;
; #pragma unroll
;         for (int bj = 0; bj < 2; ++bj)
; #pragma unroll
;             for (int n = 0; n < 2; ++n) p.bv[bj][n] = *(const f32x4*)(pb + bj * 32 + 4 * n);
;         return p;
;     }
;     __device__ __forceinline__ void init(f32x4 (&acc)[2][2][4][2], const Pre& p) const {
; #pragma unroll
;         for (int ai = 0; ai < 2; ++ai)
; #pragma unroll
;             for (int bj = 0; bj < 2; ++bj)
; #pragma unroll
;                 for (int m = 0; m < 4; ++m)
; #pragma unroll
.LBB0_1125:
	s_add_i32 s62, s62, 1
	s_lshl_b32 s1, s62, 5
	s_or_b32 s18, s1, s6
	v_cmp_ge_i32_e32 vcc, s18, v1
	v_cmp_lt_i32_e64 s[4:5], s18, v1
	s_mov_b64 s[42:43], s[46:47]
	s_mov_b64 s[40:41], s[44:45]
	s_cbranch_vccnz .LBB0_1127
	s_lshl_b32 s1, s18, 2
	s_add_i32 s1, s1, 0
	s_add_i32 s1, s1, 0x20000
	v_mov_b32_e32 v10, s1
	ds_read_b32 v10, v10
	s_lshl_b64 s[36:37], s[18:19], 19
	s_waitcnt lgkmcnt(0)
	v_readfirstlane_b32 s12, v10
	s_ashr_i32 s13, s12, 31
	s_add_u32 s40, s7, s36
	s_addc_u32 s41, s23, s37
	s_lshl_b64 s[36:37], s[12:13], 18
	s_add_u32 s42, s58, s36
	s_addc_u32 s43, s59, s37
	s_lshl_b32 s63, s18, 8
	s_mov_b64 s[36:37], s[42:43]
	s_mov_b64 s[38:39], s[40:41]
.LBB0_1127:
	s_add_u32 s44, s44, 0x80
	s_waitcnt vmcnt(0)
	v_pk_mul_f32 v[20:21], v[80:81], s[22:23] op_sel_hi:[1,0]
	v_pk_mul_f32 v[24:25], v[76:77], s[22:23] op_sel_hi:[1,0]
	v_pk_mul_f32 v[12:13], v[8:9], s[22:23] op_sel_hi:[1,0]
	v_pk_mul_f32 v[16:17], v[4:5], s[22:23] op_sel_hi:[1,0]
	s_addc_u32 s45, s45, 0
	v_pk_mul_f32 v[18:19], v[78:79], s[22:23] op_sel_hi:[1,0]
	v_pk_mul_f32 v[22:23], v[74:75], s[22:23] op_sel_hi:[1,0]
	v_pk_mul_f32 v[10:11], v[6:7], s[22:23] op_sel_hi:[1,0]
	v_pk_mul_f32 v[14:15], v[2:3], s[22:23] op_sel_hi:[1,0]
	s_add_u32 s1, s46, 0x1000000
	v_mov_b64_e32 v[28:29], v[16:17]
	v_mov_b64_e32 v[32:33], v[12:13]
	v_mov_b64_e32 v[44:45], v[16:17]
	v_mov_b64_e32 v[48:49], v[12:13]
	v_mov_b64_e32 v[60:61], v[16:17]
	v_mov_b64_e32 v[64:65], v[12:13]
	v_mov_b64_e32 v[36:37], v[24:25]
	v_mov_b64_e32 v[40:41], v[20:21]
	v_mov_b64_e32 v[52:53], v[24:25]
	v_mov_b64_e32 v[56:57], v[20:21]
	v_mov_b64_e32 v[68:69], v[24:25]
	v_mov_b64_e32 v[72:73], v[20:21]
	v_mov_b64_e32 v[84:85], v[16:17]
	v_mov_b64_e32 v[88:89], v[12:13]
	v_mov_b64_e32 v[100:101], v[16:17]
	v_mov_b64_e32 v[104:105], v[12:13]
	v_mov_b64_e32 v[116:117], v[16:17]
	v_mov_b64_e32 v[120:121], v[12:13]
	v_mov_b64_e32 v[132:133], v[16:17]
	v_mov_b64_e32 v[136:137], v[12:13]
	v_mov_b64_e32 v[92:93], v[24:25]
	v_mov_b64_e32 v[96:97], v[20:21]
	v_mov_b64_e32 v[108:109], v[24:25]
	v_mov_b64_e32 v[112:113], v[20:21]
	v_mov_b64_e32 v[124:125], v[24:25]
	v_mov_b64_e32 v[128:129], v[20:21]
	v_mov_b64_e32 v[140:141], v[24:25]
	v_mov_b64_e32 v[144:145], v[20:21]
	s_addc_u32 s13, s47, 0
	s_mov_b32 s18, -2
	v_mov_b64_e32 v[26:27], v[14:15]
	v_mov_b64_e32 v[30:31], v[10:11]
	v_mov_b64_e32 v[42:43], v[14:15]
	v_mov_b64_e32 v[46:47], v[10:11]
	v_mov_b64_e32 v[58:59], v[14:15]
	v_mov_b64_e32 v[62:63], v[10:11]
	v_mov_b64_e32 v[34:35], v[22:23]
	v_mov_b64_e32 v[38:39], v[18:19]
	v_mov_b64_e32 v[50:51], v[22:23]
	v_mov_b64_e32 v[54:55], v[18:19]
	v_mov_b64_e32 v[66:67], v[22:23]
	v_mov_b64_e32 v[70:71], v[18:19]
	v_mov_b64_e32 v[82:83], v[14:15]
	v_mov_b64_e32 v[86:87], v[10:11]
	v_mov_b64_e32 v[98:99], v[14:15]
	v_mov_b64_e32 v[102:103], v[10:11]
	v_mov_b64_e32 v[114:115], v[14:15]
	v_mov_b64_e32 v[118:119], v[10:11]
	v_mov_b64_e32 v[130:131], v[14:15]
	v_mov_b64_e32 v[134:135], v[10:11]
	v_mov_b64_e32 v[90:91], v[22:23]
	v_mov_b64_e32 v[94:95], v[18:19]
	v_mov_b64_e32 v[106:107], v[22:23]
	v_mov_b64_e32 v[110:111], v[18:19]
	v_mov_b64_e32 v[122:123], v[22:23]
	v_mov_b64_e32 v[126:127], v[18:19]
	v_mov_b64_e32 v[138:139], v[22:23]
	v_mov_b64_e32 v[142:143], v[18:19]
.LBB0_1128:
	v_add_u32_e32 v74, s60, v163
	ds_read_b128 v[2:5], v74
	ds_read_b128 v[6:9], v74 offset:1024
	ds_read_b128 v[172:175], v74 offset:2048
	ds_read_b128 v[176:179], v74 offset:3072
	v_add_u32_e32 v74, s61, v163
	ds_read_b128 v[180:183], v74
	ds_read_b128 v[184:187], v74 offset:1024
	ds_read_b128 v[188:191], v74 offset:2048
	ds_read_b128 v[192:195], v74 offset:3072
	s_add_u32 s46, s44, 0x80
	s_addc_u32 s47, s45, 0
	s_cmp_eq_u32 s18, 12
	s_cselect_b32 s49, s41, s47
	s_cselect_b32 s48, s40, s46
	s_cselect_b32 s47, s43, s13
	s_cselect_b32 s46, s42, s1
	v_lshl_add_u64 v[220:221], s[44:45], 0, v[158:159]
	s_add_i32 m0, s51, 0xc000
	ds_read_b128 v[74:77], v167
	ds_read_b128 v[78:81], v167 offset:1024
	ds_read_b128 v[196:199], v167 offset:2048
	ds_read_b128 v[200:203], v167 offset:3072
	ds_read_b128 v[204:207], v167 offset:4096
	ds_read_b128 v[208:211], v167 offset:5120
	ds_read_b128 v[212:215], v167 offset:6144
	ds_read_b128 v[216:219], v167 offset:7168
	global_load_lds_dwordx4 v[220:221], off
	v_lshl_add_u64 v[220:221], s[44:45], 0, v[160:161]
	s_add_i32 m0, s51, 0xe000
	s_nop 0
	global_load_lds_dwordx4 v[220:221], off
	s_waitcnt vmcnt(8)
	s_waitcnt lgkmcnt(0)
	s_barrier
	s_setprio 1
	s_waitcnt lgkmcnt(0)
	v_mfma_scale_f32_16x16x128_f8f6f4 v[142:145], v[2:9], v[74:81], v[142:145], v162, v162 op_sel_hi:[0,0,0]
	v_mfma_scale_f32_16x16x128_f8f6f4 v[138:141], v[172:179], v[74:81], v[138:141], v162, v162 op_sel_hi:[0,0,0]
	v_mfma_scale_f32_16x16x128_f8f6f4 v[126:129], v[2:9], v[196:203], v[126:129], v162, v162 op_sel_hi:[0,0,0]
	v_mfma_scale_f32_16x16x128_f8f6f4 v[122:125], v[172:179], v[196:203], v[122:125], v162, v162 op_sel_hi:[0,0,0]
	v_mfma_scale_f32_16x16x128_f8f6f4 v[110:113], v[2:9], v[204:211], v[110:113], v162, v162 op_sel_hi:[0,0,0]
	v_mfma_scale_f32_16x16x128_f8f6f4 v[106:109], v[172:179], v[204:211], v[106:109], v162, v162 op_sel_hi:[0,0,0]
	v_mfma_scale_f32_16x16x128_f8f6f4 v[94:97], v[2:9], v[212:219], v[94:97], v162, v162 op_sel_hi:[0,0,0]
	v_mfma_scale_f32_16x16x128_f8f6f4 v[90:93], v[172:179], v[212:219], v[90:93], v162, v162 op_sel_hi:[0,0,0]
	s_setprio 0
	s_setprio 1
	v_mfma_scale_f32_16x16x128_f8f6f4 v[134:137], v[180:187], v[74:81], v[134:137], v162, v162 op_sel_hi:[0,0,0]
	v_mfma_scale_f32_16x16x128_f8f6f4 v[130:133], v[188:195], v[74:81], v[130:133], v162, v162 op_sel_hi:[0,0,0]
	v_mfma_scale_f32_16x16x128_f8f6f4 v[118:121], v[180:187], v[196:203], v[118:121], v162, v162 op_sel_hi:[0,0,0]
	v_mfma_scale_f32_16x16x128_f8f6f4 v[114:117], v[188:195], v[196:203], v[114:117], v162, v162 op_sel_hi:[0,0,0]
	v_mfma_scale_f32_16x16x128_f8f6f4 v[102:105], v[180:187], v[204:211], v[102:105], v162, v162 op_sel_hi:[0,0,0]
	v_mfma_scale_f32_16x16x128_f8f6f4 v[98:101], v[188:195], v[204:211], v[98:101], v162, v162 op_sel_hi:[0,0,0]
	v_mfma_scale_f32_16x16x128_f8f6f4 v[86:89], v[180:187], v[212:219], v[86:89], v162, v162 op_sel_hi:[0,0,0]
	v_mfma_scale_f32_16x16x128_f8f6f4 v[82:85], v[188:195], v[212:219], v[82:85], v162, v162 op_sel_hi:[0,0,0]
	s_setprio 0
	s_barrier
; #define PG8_STAGE(bufoff, gbase, voff) do { _Pragma("unroll") for (int _i = 0; _i < 2; ++_i) \
;         __builtin_amdgcn_global_load_lds((const unsigned*)((const char*)(gbase) + (voff)[_i]), (LAS unsigned*)(lds + (bufoff) + ldsw + _i * 8192), 16, 0, 0); } while (0)
; #define PG8_LDA(dst, b, h) do { _Pragma("unroll") for (int m = 0; m < 4; ++m) { if constexpr (F8) dst##8[m] = PG8_LD32(lds + PG8_SA(b, h) + aoff + m * 2048); \
;         else { _Pragma("unroll") for (int k = 0; k < 2; ++k) dst[m][k] = *(const LAS bf16x8*)(lds + PG8_SA(b, h) + aoff + m * 2048 + k * 1024); } } } while (0)
; #define PG8_LDB(dst, b, h) do { _Pragma("unroll") for (int n = 0; n < 2; ++n) { if constexpr (F8) dst##8[n] = PG8_LD32(lds + PG8_SB(b, h) + boff + n * 2048); \
;         else { _Pragma("unroll") for (int k = 0; k < 2; ++k) dst[n][k] = *(const LAS bf16x8*)(lds + PG8_SB(b, h) + boff + n * 2048 + k * 1024); } } } while (0)
; #define PG8_WAIT_V(n) asm volatile("s_waitcnt vmcnt(" #n ")" ::: "memory")
; #define PG8_WAIT_L(n) asm volatile("s_waitcnt lgkmcnt(" #n ")" ::: "memory")
; #define PG8_BAR __builtin_amdgcn_s_barrier()
; #define PG8_SCHED __builtin_amdgcn_sched_barrier(0)
; template <class Epi, class Sched, bool GATHER, bool F8 = false>
; __device__ __forceinline__ void gemm_phase(LAS unsigned char* lds, const int K, const Sched& S, const Epi& E) {
;     ...
;             PG8_LDA(At, 0, 1); PG8_STAGE(PG8_SB(0, 0), b2, voffB); PG8_STAGE(PG8_SB(0, 1), b2 + hstepB, voffB); PG8_STAGE(PG8_SA(0, 0), a2, vN[0]);
;             PG8_WAIT_V(8); PG8_WAIT_L(0); PG8_BAR; PG8_MMA(1, 0, At, B0); PG8_MMA(1, 1, At, B1); PG8_BAR; PG8_SCHED;
;             PG8_LDB(B0, 1, 0); PG8_LDB(B1, 1, 1); PG8_SCHED; PG8_LDA(At, 1, 0); PG8_STAGE(PG8_SA(0, 1), a2, vN[1]);
;             PG8_WAIT_V(8); PG8_WAIT_L(0); PG8_BAR; PG8_MMA(0, 0, At, B0); PG8_MMA(0, 1, At, B1); PG8_BAR; PG8_SCHED;
	s_add_i32 s65, s60, s25
	v_lshl_add_u64 v[74:75], s[46:47], 0, v[156:157]
	s_mov_b32 m0, s65
	ds_read_b128 v[196:199], v167 offset:16384
	ds_read_b128 v[200:203], v167 offset:17408
	ds_read_b128 v[204:207], v167 offset:18432
	ds_read_b128 v[208:211], v167 offset:19456
	ds_read_b128 v[212:215], v167 offset:20480
	ds_read_b128 v[216:219], v167 offset:21504
	ds_read_b128 v[220:223], v167 offset:22528
	ds_read_b128 v[224:227], v167 offset:23552
	global_load_lds_dwordx4 v[74:75], off
	s_add_i32 m0, s65, 0x2000
	s_add_u32 s66, s46, 0x1000
	v_lshl_add_u64 v[76:77], s[46:47], 0, v[150:151]
	s_addc_u32 s67, s47, 0
	s_add_i32 s65, s61, s25
	global_load_lds_dwordx4 v[76:77], off
	v_lshl_add_u64 v[78:79], s[66:67], 0, v[156:157]
	s_mov_b32 m0, s65
	v_lshl_add_u64 v[80:81], s[48:49], 0, v[146:147]
	global_load_lds_dwordx4 v[78:79], off
	v_lshl_add_u64 v[78:79], s[66:67], 0, v[150:151]
	s_add_i32 m0, s65, 0x2000
	s_nop 0
	global_load_lds_dwordx4 v[78:79], off
	v_lshl_add_u64 v[78:79], s[48:49], 0, v[152:153]
	s_mov_b32 m0, s51
	s_nop 0
	global_load_lds_dwordx4 v[78:79], off
	s_mov_b32 m0, s52
	s_nop 0
	global_load_lds_dwordx4 v[80:81], off
	s_waitcnt vmcnt(8)
	s_waitcnt lgkmcnt(0)
	s_barrier
	s_setprio 1
	s_waitcnt lgkmcnt(0)
	v_mfma_scale_f32_16x16x128_f8f6f4 v[70:73], v[2:9], v[196:203], v[70:73], v162, v162 op_sel_hi:[0,0,0]
	v_mfma_scale_f32_16x16x128_f8f6f4 v[66:69], v[172:179], v[196:203], v[66:69], v162, v162 op_sel_hi:[0,0,0]
	v_mfma_scale_f32_16x16x128_f8f6f4 v[54:57], v[2:9], v[204:211], v[54:57], v162, v162 op_sel_hi:[0,0,0]
	v_mfma_scale_f32_16x16x128_f8f6f4 v[50:53], v[172:179], v[204:211], v[50:53], v162, v162 op_sel_hi:[0,0,0]
	v_mfma_scale_f32_16x16x128_f8f6f4 v[38:41], v[2:9], v[212:219], v[38:41], v162, v162 op_sel_hi:[0,0,0]
	v_mfma_scale_f32_16x16x128_f8f6f4 v[34:37], v[172:179], v[212:219], v[34:37], v162, v162 op_sel_hi:[0,0,0]
	v_mfma_scale_f32_16x16x128_f8f6f4 v[18:21], v[2:9], v[220:227], v[18:21], v162, v162 op_sel_hi:[0,0,0]
	v_mfma_scale_f32_16x16x128_f8f6f4 v[22:25], v[172:179], v[220:227], v[22:25], v162, v162 op_sel_hi:[0,0,0]
	s_setprio 0
	s_setprio 1
	v_mfma_scale_f32_16x16x128_f8f6f4 v[62:65], v[180:187], v[196:203], v[62:65], v162, v162 op_sel_hi:[0,0,0]
	v_mfma_scale_f32_16x16x128_f8f6f4 v[58:61], v[188:195], v[196:203], v[58:61], v162, v162 op_sel_hi:[0,0,0]
	v_mfma_scale_f32_16x16x128_f8f6f4 v[46:49], v[180:187], v[204:211], v[46:49], v162, v162 op_sel_hi:[0,0,0]
	v_mfma_scale_f32_16x16x128_f8f6f4 v[42:45], v[188:195], v[204:211], v[42:45], v162, v162 op_sel_hi:[0,0,0]
	v_mfma_scale_f32_16x16x128_f8f6f4 v[30:33], v[180:187], v[212:219], v[30:33], v162, v162 op_sel_hi:[0,0,0]
	v_mfma_scale_f32_16x16x128_f8f6f4 v[26:29], v[188:195], v[212:219], v[26:29], v162, v162 op_sel_hi:[0,0,0]
	v_mfma_scale_f32_16x16x128_f8f6f4 v[10:13], v[180:187], v[220:227], v[10:13], v162, v162 op_sel_hi:[0,0,0]
	v_mfma_scale_f32_16x16x128_f8f6f4 v[14:17], v[188:195], v[220:227], v[14:17], v162, v162 op_sel_hi:[0,0,0]
	s_setprio 0
	s_barrier
	s_add_i32 s65, 0, 0x18000
	s_add_i32 s66, 0, 0x1c000
	v_add_u32_e32 v2, s65, v163
	v_add_u32_e32 v192, s66, v163
	ds_read_b128 v[172:175], v2
	ds_read_b128 v[176:179], v2 offset:1024
	ds_read_b128 v[180:183], v2 offset:2048
	ds_read_b128 v[184:187], v2 offset:3072
	ds_read_b128 v[2:5], v192
	ds_read_b128 v[6:9], v192 offset:1024
	ds_read_b128 v[188:191], v192 offset:2048
	ds_read_b128 v[192:195], v192 offset:3072
	s_mov_b32 m0, s53
	v_lshl_add_u64 v[228:229], s[48:49], 0, v[154:155]
	ds_read_b128 v[196:199], v167 offset:32768
	ds_read_b128 v[200:203], v167 offset:33792
	ds_read_b128 v[204:207], v167 offset:34816
	ds_read_b128 v[208:211], v167 offset:35840
	ds_read_b128 v[212:215], v167 offset:36864
	ds_read_b128 v[216:219], v167 offset:37888
	ds_read_b128 v[220:223], v167 offset:38912
	ds_read_b128 v[224:227], v167 offset:39936
	global_load_lds_dwordx4 v[228:229], off
	v_lshl_add_u64 v[228:229], s[48:49], 0, v[148:149]
	s_mov_b32 m0, s54
	s_nop 0
	global_load_lds_dwordx4 v[228:229], off
	s_waitcnt vmcnt(8)
	s_waitcnt lgkmcnt(0)
	s_barrier
; #define PG8_STAGE(bufoff, gbase, voff) do { _Pragma("unroll") for (int _i = 0; _i < 2; ++_i) \
;         __builtin_amdgcn_global_load_lds((const unsigned*)((const char*)(gbase) + (voff)[_i]), (LAS unsigned*)(lds + (bufoff) + ldsw + _i * 8192), 16, 0, 0); } while (0)
; #define PG8_LDA(dst, b, h) do { _Pragma("unroll") for (int m = 0; m < 4; ++m) { if constexpr (F8) dst##8[m] = PG8_LD32(lds + PG8_SA(b, h) + aoff + m * 2048); \
;         else { _Pragma("unroll") for (int k = 0; k < 2; ++k) dst[m][k] = *(const LAS bf16x8*)(lds + PG8_SA(b, h) + aoff + m * 2048 + k * 1024); } } } while (0)
; #define PG8_LDB(dst, b, h) do { _Pragma("unroll") for (int n = 0; n < 2; ++n) { if constexpr (F8) dst##8[n] = PG8_LD32(lds + PG8_SB(b, h) + boff + n * 2048); \
;         else { _Pragma("unroll") for (int k = 0; k < 2; ++k) dst[n][k] = *(const LAS bf16x8*)(lds + PG8_SB(b, h) + boff + n * 2048 + k * 1024); } } } while (0)
; #define PG8_WAIT_V(n) asm volatile("s_waitcnt vmcnt(" #n ")" ::: "memory")
; #define PG8_WAIT_L(n) asm volatile("s_waitcnt lgkmcnt(" #n ")" ::: "memory")
; #define PG8_BAR __builtin_amdgcn_s_barrier()
; #define PG8_SCHED __builtin_amdgcn_sched_barrier(0)
; template <class Epi, class Sched, bool GATHER, bool F8 = false>
; __device__ __forceinline__ void gemm_phase(LAS unsigned char* lds, const int K, const Sched& S, const Epi& E) {
;     ...
;             PG8_LDB(B0, 1, 0); PG8_LDB(B1, 1, 1); PG8_SCHED; PG8_LDA(At, 1, 0); PG8_STAGE(PG8_SA(0, 1), a2, vN[1]);
;             PG8_WAIT_V(8); PG8_WAIT_L(0); PG8_BAR; PG8_MMA(0, 0, At, B0); PG8_MMA(0, 1, At, B1); PG8_BAR; PG8_SCHED;
;             PG8_LDA(At, 1, 1); PG8_STAGE(PG8_SB(1, 0), b3, voffB); PG8_STAGE(PG8_SB(1, 1), b3 + hstepB, voffB); PG8_STAGE(PG8_SA(1, 0), a3, vN[0]);
;             PG8_WAIT_V(8); PG8_WAIT_L(0); PG8_BAR; PG8_MMA(1, 0, At, B0); PG8_MMA(1, 1, At, B1); PG8_BAR; PG8_SCHED;
;         }
	s_setprio 1
	s_waitcnt lgkmcnt(0)
	v_mfma_scale_f32_16x16x128_f8f6f4 v[142:145], v[172:179], v[196:203], v[142:145], v162, v162 op_sel_hi:[0,0,0]
	v_mfma_scale_f32_16x16x128_f8f6f4 v[138:141], v[180:187], v[196:203], v[138:141], v162, v162 op_sel_hi:[0,0,0]
	v_mfma_scale_f32_16x16x128_f8f6f4 v[126:129], v[172:179], v[204:211], v[126:129], v162, v162 op_sel_hi:[0,0,0]
	v_mfma_scale_f32_16x16x128_f8f6f4 v[122:125], v[180:187], v[204:211], v[122:125], v162, v162 op_sel_hi:[0,0,0]
	v_mfma_scale_f32_16x16x128_f8f6f4 v[110:113], v[172:179], v[212:219], v[110:113], v162, v162 op_sel_hi:[0,0,0]
	v_mfma_scale_f32_16x16x128_f8f6f4 v[106:109], v[180:187], v[212:219], v[106:109], v162, v162 op_sel_hi:[0,0,0]
	v_mfma_scale_f32_16x16x128_f8f6f4 v[94:97], v[172:179], v[220:227], v[94:97], v162, v162 op_sel_hi:[0,0,0]
	v_mfma_scale_f32_16x16x128_f8f6f4 v[90:93], v[180:187], v[220:227], v[90:93], v162, v162 op_sel_hi:[0,0,0]
	s_setprio 0
	s_setprio 1
	v_mfma_scale_f32_16x16x128_f8f6f4 v[134:137], v[2:9], v[196:203], v[134:137], v162, v162 op_sel_hi:[0,0,0]
	v_mfma_scale_f32_16x16x128_f8f6f4 v[130:133], v[188:195], v[196:203], v[130:133], v162, v162 op_sel_hi:[0,0,0]
	v_mfma_scale_f32_16x16x128_f8f6f4 v[118:121], v[2:9], v[204:211], v[118:121], v162, v162 op_sel_hi:[0,0,0]
	v_mfma_scale_f32_16x16x128_f8f6f4 v[114:117], v[188:195], v[204:211], v[114:117], v162, v162 op_sel_hi:[0,0,0]
	v_mfma_scale_f32_16x16x128_f8f6f4 v[102:105], v[2:9], v[212:219], v[102:105], v162, v162 op_sel_hi:[0,0,0]
	v_mfma_scale_f32_16x16x128_f8f6f4 v[98:101], v[188:195], v[212:219], v[98:101], v162, v162 op_sel_hi:[0,0,0]
	v_mfma_scale_f32_16x16x128_f8f6f4 v[86:89], v[2:9], v[220:227], v[86:89], v162, v162 op_sel_hi:[0,0,0]
	v_mfma_scale_f32_16x16x128_f8f6f4 v[82:85], v[188:195], v[220:227], v[82:85], v162, v162 op_sel_hi:[0,0,0]
	s_setprio 0
	s_barrier
	s_add_i32 s48, s65, s25
	v_lshl_add_u64 v[74:75], v[74:75], 0, s[100:101]
	s_mov_b32 m0, s48
	ds_read_b128 v[196:199], v167 offset:49152
	ds_read_b128 v[200:203], v167 offset:50176
	ds_read_b128 v[204:207], v167 offset:51200
	ds_read_b128 v[208:211], v167 offset:52224
	ds_read_b128 v[212:215], v167 offset:53248
	ds_read_b128 v[216:219], v167 offset:54272
	ds_read_b128 v[220:223], v167 offset:55296
	ds_read_b128 v[224:227], v167 offset:56320
	global_load_lds_dwordx4 v[74:75], off
	s_add_i32 m0, s48, 0x2000
	s_add_u32 s46, s46, 0x801000
	v_lshl_add_u64 v[74:75], v[76:77], 0, s[100:101]
	s_addc_u32 s47, s47, 0
	s_add_i32 s48, s66, s25
	global_load_lds_dwordx4 v[74:75], off
	v_lshl_add_u64 v[74:75], s[46:47], 0, v[156:157]
	s_mov_b32 m0, s48
	s_nop 0
	global_load_lds_dwordx4 v[74:75], off
	v_lshl_add_u64 v[74:75], s[46:47], 0, v[150:151]
	s_add_i32 m0, s48, 0x2000
	s_nop 0
	global_load_lds_dwordx4 v[74:75], off
	v_lshl_add_u64 v[74:75], v[78:79], 0, s[16:17]
	s_mov_b32 m0, s56
	s_nop 0
	global_load_lds_dwordx4 v[74:75], off
	v_lshl_add_u64 v[74:75], v[80:81], 0, s[16:17]
	s_mov_b32 m0, s57
	s_nop 0
	global_load_lds_dwordx4 v[74:75], off
	s_waitcnt vmcnt(8)
	s_waitcnt lgkmcnt(0)
	s_barrier
	s_setprio 1
	s_waitcnt lgkmcnt(0)
	v_mfma_scale_f32_16x16x128_f8f6f4 v[70:73], v[172:179], v[196:203], v[70:73], v162, v162 op_sel_hi:[0,0,0]
	v_mfma_scale_f32_16x16x128_f8f6f4 v[66:69], v[180:187], v[196:203], v[66:69], v162, v162 op_sel_hi:[0,0,0]
	v_mfma_scale_f32_16x16x128_f8f6f4 v[54:57], v[172:179], v[204:211], v[54:57], v162, v162 op_sel_hi:[0,0,0]
	v_mfma_scale_f32_16x16x128_f8f6f4 v[50:53], v[180:187], v[204:211], v[50:53], v162, v162 op_sel_hi:[0,0,0]
	v_mfma_scale_f32_16x16x128_f8f6f4 v[38:41], v[172:179], v[212:219], v[38:41], v162, v162 op_sel_hi:[0,0,0]
	v_mfma_scale_f32_16x16x128_f8f6f4 v[34:37], v[180:187], v[212:219], v[34:37], v162, v162 op_sel_hi:[0,0,0]
	v_mfma_scale_f32_16x16x128_f8f6f4 v[18:21], v[172:179], v[220:227], v[18:21], v162, v162 op_sel_hi:[0,0,0]
	v_mfma_scale_f32_16x16x128_f8f6f4 v[22:25], v[180:187], v[220:227], v[22:25], v162, v162 op_sel_hi:[0,0,0]
	s_setprio 0
	s_setprio 1
	v_mfma_scale_f32_16x16x128_f8f6f4 v[62:65], v[2:9], v[196:203], v[62:65], v162, v162 op_sel_hi:[0,0,0]
	v_mfma_scale_f32_16x16x128_f8f6f4 v[58:61], v[188:195], v[196:203], v[58:61], v162, v162 op_sel_hi:[0,0,0]
	v_mfma_scale_f32_16x16x128_f8f6f4 v[46:49], v[2:9], v[204:211], v[46:49], v162, v162 op_sel_hi:[0,0,0]
	v_mfma_scale_f32_16x16x128_f8f6f4 v[42:45], v[188:195], v[204:211], v[42:45], v162, v162 op_sel_hi:[0,0,0]
	v_mfma_scale_f32_16x16x128_f8f6f4 v[30:33], v[2:9], v[212:219], v[30:33], v162, v162 op_sel_hi:[0,0,0]
	v_mfma_scale_f32_16x16x128_f8f6f4 v[26:29], v[188:195], v[212:219], v[26:29], v162, v162 op_sel_hi:[0,0,0]
	v_mfma_scale_f32_16x16x128_f8f6f4 v[10:13], v[2:9], v[220:227], v[10:13], v162, v162 op_sel_hi:[0,0,0]
	v_mfma_scale_f32_16x16x128_f8f6f4 v[14:17], v[188:195], v[220:227], v[14:17], v162, v162 op_sel_hi:[0,0,0]
	s_setprio 0
	s_barrier
	s_add_i32 s18, s18, 2
	s_add_u32 s44, s44, 0x100
	s_addc_u32 s45, s45, 0
	s_add_u32 s1, s1, 0x1000000
	s_addc_u32 s13, s13, 0
	s_cmp_gt_u32 s18, 13
	s_cbranch_scc0 .LBB0_1128
	s_and_b64 vcc, exec, s[20:21]
	s_cbranch_vccz .LBB0_1131
	s_barrier
